# baseline (speedup 1.0000x reference)
.LBB2_10:
	s_or_b64 exec, exec, s[14:15]
	v_lshrrev_b32_e32 v45, 2, v44
	s_lshl_b64 s[0:1], s[2:3], 2
	v_and_or_b32 v45, v45, 12, s18
	s_waitcnt lgkmcnt(0)
	s_add_u32 s18, s8, s0
	s_addc_u32 s19, s9, s1
	s_waitcnt lgkmcnt(0)
	s_barrier
	v_lshlrev_b32_e32 v124, 2, v45
	s_add_u32 s20, s10, s0
	v_mov_b64_e32 v[116:117], v[196:197]
	v_mov_b64_e32 v[118:119], v[198:199]
	s_addc_u32 s21, s11, s1
	v_mov_b64_e32 v[112:113], v[200:201]
	v_mov_b64_e32 v[114:115], v[202:203]
	v_and_or_b32 v44, v44, 15, s16
	s_movk_i32 s7, 0x190
	v_lshl_add_u32 v46, v44, 3, 0
	v_mul_lo_u32 v104, v44, s7
	v_add_u32_e32 v44, 0xc800, v46
	v_lshlrev_b32_e32 v105, 1, v45
	ds_read2_b64 v[60:63], v44 offset1:16
	ds_read2_b64 v[44:47], v44 offset0:32 offset1:48
	v_add3_u32 v121, 0, v105, v104
	v_mov_b64_e32 v[108:109], v[204:205]
	v_mov_b64_e32 v[110:111], v[206:207]
	v_mov_b64_e32 v[104:105], v[208:209]
	v_mov_b64_e32 v[106:107], v[210:211]
	s_mov_b32 s8, 0x3e6d3388
	s_mov_b32 s22, 0xbf3a00e3
	s_mov_b32 s0, 0x3f07dc22
	s_mov_b32 s16, 0xbf38aa3b
	v_mov_b64_e32 v[122:123], s[22:23]
	s_mov_b32 s14, 0x3f35f0e3
	s_mov_b32 s6, 0xbe11a98e
	s_mov_b32 s10, 0x3e027906
	s_waitcnt vmcnt(3) lgkmcnt(1)
	v_pk_fma_f32 v[100:101], v[116:117], v[60:61], v[100:101] op_sel_hi:[1,0,1] neg_lo:[1,0,0] neg_hi:[1,0,0]
	v_xor_b32_e32 v119, 0x80000000, v119
	v_xor_b32_e32 v118, 0x80000000, v118
	v_pk_fma_f32 v[102:103], v[118:119], v[60:61], v[102:103] op_sel_hi:[1,0,1]
	s_waitcnt vmcnt(2)
	v_pk_fma_f32 v[100:101], v[60:61], v[100:101], v[112:113] op_sel:[1,0,0]
	v_pk_fma_f32 v[102:103], v[60:61], v[102:103], v[114:115] op_sel:[1,0,0]
	v_and_b32_e32 v127, 0x7fffffff, v101
	v_and_b32_e32 v126, 0x7fffffff, v100
	v_and_b32_e32 v133, 0x7fffffff, v103
	v_and_b32_e32 v132, 0x7fffffff, v102
	v_pk_fma_f32 v[126:127], v[126:127], s[8:9], 1.0 op_sel_hi:[1,0,0]
	v_pk_fma_f32 v[96:97], v[116:117], v[62:63], v[96:97] op_sel_hi:[1,0,1] neg_lo:[1,0,0] neg_hi:[1,0,0]
	v_pk_fma_f32 v[132:133], v[132:133], s[8:9], 1.0 op_sel_hi:[1,0,0]
	v_rcp_f32_e32 v126, v126
	v_rcp_f32_e32 v127, v127
	v_pk_fma_f32 v[96:97], v[62:63], v[96:97], v[112:113] op_sel:[1,0,0]
	v_rcp_f32_e32 v132, v132
	v_rcp_f32_e32 v133, v133
	v_and_b32_e32 v135, 0x7fffffff, v97
	v_and_b32_e32 v134, 0x7fffffff, v96
	v_pk_mul_f32 v[130:131], v[100:101], v[100:101]
	v_pk_fma_f32 v[134:135], v[134:135], s[8:9], 1.0 op_sel_hi:[1,0,0]
	v_pk_mul_f32 v[128:129], v[102:103], v[102:103]
	v_pk_mul_f32 v[130:131], v[130:131], s[16:17] op_sel_hi:[1,0]
	v_rcp_f32_e32 v134, v134
	v_rcp_f32_e32 v135, v135
	v_pk_fma_f32 v[140:141], v[126:127], s[0:1], v[122:123] op_sel_hi:[1,0,0]
	v_pk_mul_f32 v[128:129], v[128:129], s[16:17] op_sel_hi:[1,0]
	v_exp_f32_e32 v130, v130
	v_exp_f32_e32 v131, v131
	v_pk_fma_f32 v[142:143], v[132:133], s[0:1], v[122:123] op_sel_hi:[1,0,0]
	v_pk_fma_f32 v[140:141], v[126:127], v[140:141], s[14:15] op_sel_hi:[1,1,0]
	v_exp_f32_e32 v128, v128
	v_exp_f32_e32 v129, v129
	v_pk_fma_f32 v[142:143], v[132:133], v[142:143], s[14:15] op_sel_hi:[1,1,0]
	v_pk_fma_f32 v[140:141], v[126:127], v[140:141], s[6:7] op_sel_hi:[1,1,0]
	v_pk_mul_f32 v[138:139], v[96:97], v[96:97]
	v_pk_fma_f32 v[142:143], v[132:133], v[142:143], s[6:7] op_sel_hi:[1,1,0]
	v_pk_fma_f32 v[140:141], v[126:127], v[140:141], s[10:11] op_sel_hi:[1,1,0]
	v_pk_mul_f32 v[138:139], v[138:139], s[16:17] op_sel_hi:[1,0]
	v_pk_fma_f32 v[144:145], v[134:135], s[0:1], v[122:123] op_sel_hi:[1,0,0]
	v_pk_fma_f32 v[142:143], v[132:133], v[142:143], s[10:11] op_sel_hi:[1,1,0]
	v_pk_mul_f32 v[126:127], v[126:127], v[140:141]
	v_exp_f32_e32 v138, v138
	v_exp_f32_e32 v139, v139
	v_pk_fma_f32 v[144:145], v[134:135], v[144:145], s[14:15] op_sel_hi:[1,1,0]
	v_pk_mul_f32 v[132:133], v[132:133], v[142:143]
	v_pk_mul_f32 v[126:127], v[130:131], v[126:127]
	v_pk_fma_f32 v[98:99], v[118:119], v[62:63], v[98:99] op_sel_hi:[1,0,1]
	v_pk_fma_f32 v[144:145], v[134:135], v[144:145], s[6:7] op_sel_hi:[1,1,0]
	v_pk_mul_f32 v[128:129], v[128:129], v[132:133]
	v_pk_mul_f32 v[132:133], v[100:101], v[126:127]
	v_pk_fma_f32 v[126:127], v[100:101], v[126:127], v[100:101] neg_lo:[1,0,0] neg_hi:[1,0,0]
	v_cmp_gt_f32_e32 vcc, 0, v100
	v_pk_fma_f32 v[98:99], v[62:63], v[98:99], v[114:115] op_sel:[1,0,0]
	v_pk_fma_f32 v[144:145], v[134:135], v[144:145], s[10:11] op_sel_hi:[1,1,0]
	v_cndmask_b32_e32 v100, v126, v132, vcc
	v_cmp_gt_f32_e32 vcc, 0, v101
	v_pk_mul_f32 v[134:135], v[134:135], v[144:145]
	v_and_b32_e32 v126, 0x7fffffff, v98
	v_cndmask_b32_e32 v101, v127, v133, vcc
	v_and_b32_e32 v127, 0x7fffffff, v99
	v_pk_mul_f32 v[130:131], v[138:139], v[134:135]
	v_pk_mul_f32 v[134:135], v[102:103], v[128:129]
	v_pk_fma_f32 v[128:129], v[102:103], v[128:129], v[102:103] neg_lo:[1,0,0] neg_hi:[1,0,0]
	v_cmp_gt_f32_e32 vcc, 0, v102
	v_pk_fma_f32 v[126:127], v[126:127], s[8:9], 1.0 op_sel_hi:[1,0,0]
	v_pk_mul_f32 v[138:139], v[96:97], v[130:131]
	v_cndmask_b32_e32 v102, v128, v134, vcc
	v_cmp_gt_f32_e32 vcc, 0, v103
	v_rcp_f32_e32 v126, v126
	v_rcp_f32_e32 v127, v127
	v_cndmask_b32_e32 v103, v129, v135, vcc
	v_cvt_pk_f16_f32 v100, v100, v101
	v_cvt_pk_f16_f32 v101, v102, v103
	v_pk_fma_f32 v[102:103], v[96:97], v[130:131], v[96:97] neg_lo:[1,0,0] neg_hi:[1,0,0]
	v_cmp_gt_f32_e32 vcc, 0, v96
	v_pk_mul_f32 v[136:137], v[98:99], v[98:99]
	s_waitcnt lgkmcnt(0)
	v_pk_fma_f32 v[92:93], v[116:117], v[44:45], v[92:93] op_sel_hi:[1,0,1] neg_lo:[1,0,0] neg_hi:[1,0,0]
	v_cndmask_b32_e32 v125, v102, v138, vcc
	v_cmp_gt_f32_e32 vcc, 0, v97
	v_pk_fma_f32 v[96:97], v[126:127], s[0:1], v[122:123] op_sel_hi:[1,0,0]
	v_pk_fma_f32 v[92:93], v[44:45], v[92:93], v[112:113] op_sel:[1,0,0]
	v_cndmask_b32_e32 v128, v103, v139, vcc
	v_pk_mul_f32 v[102:103], v[136:137], s[16:17] op_sel_hi:[1,0]
	v_pk_fma_f32 v[96:97], v[126:127], v[96:97], s[14:15] op_sel_hi:[1,1,0]
	v_exp_f32_e32 v102, v102
	v_exp_f32_e32 v103, v103
	v_pk_fma_f32 v[96:97], v[126:127], v[96:97], s[6:7] op_sel_hi:[1,1,0]
	v_cmp_gt_f32_e32 vcc, 0, v98
	v_pk_fma_f32 v[96:97], v[126:127], v[96:97], s[10:11] op_sel_hi:[1,1,0]
	v_pk_fma_f32 v[94:95], v[118:119], v[44:45], v[94:95] op_sel_hi:[1,0,1]
	v_pk_mul_f32 v[96:97], v[126:127], v[96:97]
	v_pk_mul_f32 v[126:127], v[92:93], v[92:93]
	v_pk_mul_f32 v[96:97], v[102:103], v[96:97]
	v_pk_mul_f32 v[126:127], v[126:127], s[16:17] op_sel_hi:[1,0]
	v_pk_mul_f32 v[102:103], v[98:99], v[96:97]
	v_pk_fma_f32 v[96:97], v[98:99], v[96:97], v[98:99] neg_lo:[1,0,0] neg_hi:[1,0,0]
	v_and_b32_e32 v98, 0x7fffffff, v92
	v_cndmask_b32_e32 v102, v96, v102, vcc
	v_cmp_gt_f32_e32 vcc, 0, v99
	v_and_b32_e32 v99, 0x7fffffff, v93
	v_pk_fma_f32 v[98:99], v[98:99], s[8:9], 1.0 op_sel_hi:[1,0,0]
	v_cndmask_b32_e32 v97, v97, v103, vcc
	v_rcp_f32_e32 v98, v98
	v_rcp_f32_e32 v99, v99
	v_cvt_pk_f16_f32 v97, v102, v97
	v_pk_fma_f32 v[94:95], v[44:45], v[94:95], v[114:115] op_sel:[1,0,0]
	v_exp_f32_e32 v126, v126
	v_pk_fma_f32 v[102:103], v[98:99], s[0:1], v[122:123] op_sel_hi:[1,0,0]
	v_exp_f32_e32 v127, v127
	v_pk_fma_f32 v[102:103], v[98:99], v[102:103], s[14:15] op_sel_hi:[1,1,0]
	v_cvt_pk_f16_f32 v96, v125, v128
	v_pk_fma_f32 v[102:103], v[98:99], v[102:103], s[6:7] op_sel_hi:[1,1,0]
	v_and_b32_e32 v129, 0x7fffffff, v95
	v_and_b32_e32 v128, 0x7fffffff, v94
	v_pk_fma_f32 v[102:103], v[98:99], v[102:103], s[10:11] op_sel_hi:[1,1,0]
	v_pk_fma_f32 v[128:129], v[128:129], s[8:9], 1.0 op_sel_hi:[1,0,0]
	v_pk_mul_f32 v[98:99], v[98:99], v[102:103]
	v_rcp_f32_e32 v128, v128
	v_rcp_f32_e32 v129, v129
	v_pk_mul_f32 v[98:99], v[126:127], v[98:99]
	v_cmp_gt_f32_e32 vcc, 0, v92
	v_pk_mul_f32 v[126:127], v[92:93], v[98:99]
	v_pk_fma_f32 v[98:99], v[92:93], v[98:99], v[92:93] neg_lo:[1,0,0] neg_hi:[1,0,0]
	v_pk_mul_f32 v[102:103], v[94:95], v[94:95]
	v_cndmask_b32_e32 v125, v98, v126, vcc
	v_cmp_gt_f32_e32 vcc, 0, v93
	v_pk_fma_f32 v[92:93], v[128:129], s[0:1], v[122:123] op_sel_hi:[1,0,0]
	v_pk_fma_f32 v[88:89], v[116:117], v[46:47], v[88:89] op_sel_hi:[1,0,1] neg_lo:[1,0,0] neg_hi:[1,0,0]
	v_cndmask_b32_e32 v126, v99, v127, vcc
	v_pk_mul_f32 v[98:99], v[102:103], s[16:17] op_sel_hi:[1,0]
	v_pk_fma_f32 v[92:93], v[128:129], v[92:93], s[14:15] op_sel_hi:[1,1,0]
	v_exp_f32_e32 v98, v98
	v_exp_f32_e32 v99, v99
	v_pk_fma_f32 v[92:93], v[128:129], v[92:93], s[6:7] op_sel_hi:[1,1,0]
	v_cmp_gt_f32_e32 vcc, 0, v94
	v_pk_fma_f32 v[92:93], v[128:129], v[92:93], s[10:11] op_sel_hi:[1,1,0]
	v_pk_fma_f32 v[88:89], v[46:47], v[88:89], v[112:113] op_sel:[1,0,0]
	v_pk_mul_f32 v[92:93], v[128:129], v[92:93]
	v_pk_mul_f32 v[102:103], v[88:89], v[88:89]
	v_pk_mul_f32 v[92:93], v[98:99], v[92:93]
	v_pk_fma_f32 v[90:91], v[118:119], v[46:47], v[90:91] op_sel_hi:[1,0,1]
	v_pk_mul_f32 v[98:99], v[94:95], v[92:93]
	v_pk_fma_f32 v[92:93], v[94:95], v[92:93], v[94:95] neg_lo:[1,0,0] neg_hi:[1,0,0]
	v_and_b32_e32 v94, 0x7fffffff, v88
	v_cndmask_b32_e32 v98, v92, v98, vcc
	v_cmp_gt_f32_e32 vcc, 0, v95
	v_and_b32_e32 v95, 0x7fffffff, v89
	v_pk_fma_f32 v[94:95], v[94:95], s[8:9], 1.0 op_sel_hi:[1,0,0]
	v_cndmask_b32_e32 v93, v93, v99, vcc
	v_rcp_f32_e32 v94, v94
	v_rcp_f32_e32 v95, v95
	v_cvt_pk_f16_f32 v93, v98, v93
	v_pk_mul_f32 v[102:103], v[102:103], s[16:17] op_sel_hi:[1,0]
	v_pk_fma_f32 v[90:91], v[46:47], v[90:91], v[114:115] op_sel:[1,0,0]
	v_pk_fma_f32 v[98:99], v[94:95], s[0:1], v[122:123] op_sel_hi:[1,0,0]
	v_exp_f32_e32 v102, v102
	v_pk_fma_f32 v[98:99], v[94:95], v[98:99], s[14:15] op_sel_hi:[1,1,0]
	v_exp_f32_e32 v103, v103
	v_pk_fma_f32 v[98:99], v[94:95], v[98:99], s[6:7] op_sel_hi:[1,1,0]
	v_and_b32_e32 v113, 0x7fffffff, v91
	v_and_b32_e32 v112, 0x7fffffff, v90
	v_pk_fma_f32 v[98:99], v[94:95], v[98:99], s[10:11] op_sel_hi:[1,1,0]
	v_pk_fma_f32 v[112:113], v[112:113], s[8:9], 1.0 op_sel_hi:[1,0,0]
	v_pk_mul_f32 v[94:95], v[94:95], v[98:99]
	v_rcp_f32_e32 v112, v112
	v_rcp_f32_e32 v113, v113
	v_pk_mul_f32 v[94:95], v[102:103], v[94:95]
	v_cmp_gt_f32_e32 vcc, 0, v88
	v_pk_mul_f32 v[102:103], v[88:89], v[94:95]
	v_pk_fma_f32 v[94:95], v[88:89], v[94:95], v[88:89] neg_lo:[1,0,0] neg_hi:[1,0,0]
	v_pk_mul_f32 v[98:99], v[90:91], v[90:91]
	v_cndmask_b32_e32 v102, v94, v102, vcc
	v_cmp_gt_f32_e32 vcc, 0, v89
	v_pk_fma_f32 v[88:89], v[112:113], s[0:1], v[122:123] op_sel_hi:[1,0,0]
	s_waitcnt vmcnt(1)
	v_pk_fma_f32 v[84:85], v[108:109], v[60:61], v[84:85] op_sel_hi:[1,0,1] neg_lo:[1,0,0] neg_hi:[1,0,0]
	v_cndmask_b32_e32 v103, v95, v103, vcc
	v_pk_mul_f32 v[94:95], v[98:99], s[16:17] op_sel_hi:[1,0]
	v_pk_fma_f32 v[88:89], v[112:113], v[88:89], s[14:15] op_sel_hi:[1,1,0]
	v_exp_f32_e32 v94, v94
	v_exp_f32_e32 v95, v95
	v_pk_fma_f32 v[88:89], v[112:113], v[88:89], s[6:7] op_sel_hi:[1,1,0]
	v_cmp_gt_f32_e32 vcc, 0, v90
	v_pk_fma_f32 v[88:89], v[112:113], v[88:89], s[10:11] op_sel_hi:[1,1,0]
	s_waitcnt vmcnt(0)
	v_pk_fma_f32 v[84:85], v[60:61], v[84:85], v[104:105] op_sel:[1,0,0]
	v_pk_mul_f32 v[88:89], v[112:113], v[88:89]
	v_pk_fma_f32 v[80:81], v[108:109], v[62:63], v[80:81] op_sel_hi:[1,0,1] neg_lo:[1,0,0] neg_hi:[1,0,0]
	v_pk_mul_f32 v[88:89], v[94:95], v[88:89]
	v_pk_fma_f32 v[80:81], v[62:63], v[80:81], v[104:105] op_sel:[1,0,0]
	v_pk_mul_f32 v[94:95], v[90:91], v[88:89]
	v_pk_fma_f32 v[88:89], v[90:91], v[88:89], v[90:91] neg_lo:[1,0,0] neg_hi:[1,0,0]
	v_pk_fma_f32 v[76:77], v[108:109], v[44:45], v[76:77] op_sel_hi:[1,0,1] neg_lo:[1,0,0] neg_hi:[1,0,0]
	v_cndmask_b32_e32 v90, v88, v94, vcc
	v_cmp_gt_f32_e32 vcc, 0, v91
	v_and_b32_e32 v94, 0x7fffffff, v84
	v_cvt_pk_f16_f32 v88, v102, v103
	v_cndmask_b32_e32 v89, v89, v95, vcc
	v_and_b32_e32 v95, 0x7fffffff, v85
	v_pk_fma_f32 v[94:95], v[94:95], s[8:9], 1.0 op_sel_hi:[1,0,0]
	v_cvt_pk_f16_f32 v89, v90, v89
	v_rcp_f32_e32 v94, v94
	v_rcp_f32_e32 v95, v95
	v_xor_b32_e32 v91, 0x80000000, v111
	v_xor_b32_e32 v90, 0x80000000, v110
	v_pk_mul_f32 v[102:103], v[84:85], v[84:85]
	v_pk_fma_f32 v[86:87], v[90:91], v[60:61], v[86:87] op_sel_hi:[1,0,1]
	v_pk_fma_f32 v[98:99], v[94:95], s[0:1], v[122:123] op_sel_hi:[1,0,0]
	v_pk_mul_f32 v[102:103], v[102:103], s[16:17] op_sel_hi:[1,0]
	v_pk_fma_f32 v[86:87], v[60:61], v[86:87], v[106:107] op_sel:[1,0,0]
	v_pk_fma_f32 v[98:99], v[94:95], v[98:99], s[14:15] op_sel_hi:[1,1,0]
	v_exp_f32_e32 v102, v102
	v_exp_f32_e32 v103, v103
	v_pk_fma_f32 v[98:99], v[94:95], v[98:99], s[6:7] op_sel_hi:[1,1,0]
	v_and_b32_e32 v111, 0x7fffffff, v87
	v_and_b32_e32 v110, 0x7fffffff, v86
	v_pk_fma_f32 v[98:99], v[94:95], v[98:99], s[10:11] op_sel_hi:[1,1,0]
	v_pk_fma_f32 v[110:111], v[110:111], s[8:9], 1.0 op_sel_hi:[1,0,0]
	v_pk_mul_f32 v[94:95], v[94:95], v[98:99]
	v_rcp_f32_e32 v110, v110
	v_rcp_f32_e32 v111, v111
	v_pk_mul_f32 v[94:95], v[102:103], v[94:95]
	v_cmp_gt_f32_e32 vcc, 0, v84
	v_pk_mul_f32 v[102:103], v[84:85], v[94:95]
	v_pk_fma_f32 v[94:95], v[84:85], v[94:95], v[84:85] neg_lo:[1,0,0] neg_hi:[1,0,0]
	v_pk_mul_f32 v[98:99], v[86:87], v[86:87]
	v_cndmask_b32_e32 v102, v94, v102, vcc
	v_cmp_gt_f32_e32 vcc, 0, v85
	v_pk_fma_f32 v[84:85], v[110:111], s[0:1], v[122:123] op_sel_hi:[1,0,0]
	v_pk_fma_f32 v[82:83], v[90:91], v[62:63], v[82:83] op_sel_hi:[1,0,1]
	v_cndmask_b32_e32 v103, v95, v103, vcc
	v_pk_mul_f32 v[94:95], v[98:99], s[16:17] op_sel_hi:[1,0]
	v_pk_fma_f32 v[84:85], v[110:111], v[84:85], s[14:15] op_sel_hi:[1,1,0]
	v_exp_f32_e32 v94, v94
	v_exp_f32_e32 v95, v95
	v_pk_fma_f32 v[84:85], v[110:111], v[84:85], s[6:7] op_sel_hi:[1,1,0]
	v_cmp_gt_f32_e32 vcc, 0, v86
	v_pk_fma_f32 v[84:85], v[110:111], v[84:85], s[10:11] op_sel_hi:[1,1,0]
	v_pk_fma_f32 v[82:83], v[62:63], v[82:83], v[106:107] op_sel:[1,0,0]
	v_pk_mul_f32 v[84:85], v[110:111], v[84:85]
	v_and_b32_e32 v99, 0x7fffffff, v83
	v_pk_mul_f32 v[84:85], v[94:95], v[84:85]
	v_and_b32_e32 v98, 0x7fffffff, v82
	v_pk_mul_f32 v[94:95], v[86:87], v[84:85]
	v_pk_fma_f32 v[84:85], v[86:87], v[84:85], v[86:87] neg_lo:[1,0,0] neg_hi:[1,0,0]
	v_pk_fma_f32 v[98:99], v[98:99], s[8:9], 1.0 op_sel_hi:[1,0,0]
	v_cndmask_b32_e32 v86, v84, v94, vcc
	v_cmp_gt_f32_e32 vcc, 0, v87
	v_and_b32_e32 v87, 0x7fffffff, v81
	v_cvt_pk_f16_f32 v84, v102, v103
	v_cndmask_b32_e32 v85, v85, v95, vcc
	v_cvt_pk_f16_f32 v85, v86, v85
	v_and_b32_e32 v86, 0x7fffffff, v80
	v_pk_fma_f32 v[86:87], v[86:87], s[8:9], 1.0 op_sel_hi:[1,0,0]
	v_pk_mul_f32 v[94:95], v[80:81], v[80:81]
	v_rcp_f32_e32 v86, v86
	v_rcp_f32_e32 v87, v87
	ds_write2_b64 v121, v[100:101], v[84:85] offset1:4
	v_pk_mul_f32 v[94:95], v[94:95], s[16:17] op_sel_hi:[1,0]
	v_rcp_f32_e32 v98, v98
	v_pk_fma_f32 v[84:85], v[86:87], s[0:1], v[122:123] op_sel_hi:[1,0,0]
	v_exp_f32_e32 v94, v94
	v_pk_fma_f32 v[84:85], v[86:87], v[84:85], s[14:15] op_sel_hi:[1,1,0]
	v_exp_f32_e32 v95, v95
	v_pk_fma_f32 v[84:85], v[86:87], v[84:85], s[6:7] op_sel_hi:[1,1,0]
	v_rcp_f32_e32 v99, v99
	v_pk_fma_f32 v[84:85], v[86:87], v[84:85], s[10:11] op_sel_hi:[1,1,0]
	v_cmp_gt_f32_e32 vcc, 0, v80
	v_pk_mul_f32 v[84:85], v[86:87], v[84:85]
	v_pk_mul_f32 v[86:87], v[82:83], v[82:83]
	v_pk_mul_f32 v[84:85], v[94:95], v[84:85]
	v_pk_fma_f32 v[76:77], v[44:45], v[76:77], v[104:105] op_sel:[1,0,0]
	v_pk_mul_f32 v[94:95], v[80:81], v[84:85]
	v_pk_fma_f32 v[84:85], v[80:81], v[84:85], v[80:81] neg_lo:[1,0,0] neg_hi:[1,0,0]
	v_pk_fma_f32 v[78:79], v[90:91], v[44:45], v[78:79] op_sel_hi:[1,0,1]
	v_cndmask_b32_e32 v94, v84, v94, vcc
	v_cmp_gt_f32_e32 vcc, 0, v81
	v_pk_fma_f32 v[80:81], v[98:99], s[0:1], v[122:123] op_sel_hi:[1,0,0]
	v_pk_fma_f32 v[78:79], v[44:45], v[78:79], v[106:107] op_sel:[1,0,0]
	v_cndmask_b32_e32 v95, v85, v95, vcc
	v_pk_mul_f32 v[84:85], v[86:87], s[16:17] op_sel_hi:[1,0]
	v_pk_fma_f32 v[80:81], v[98:99], v[80:81], s[14:15] op_sel_hi:[1,1,0]
	v_exp_f32_e32 v84, v84
	v_exp_f32_e32 v85, v85
	v_pk_fma_f32 v[80:81], v[98:99], v[80:81], s[6:7] op_sel_hi:[1,1,0]
	v_cmp_gt_f32_e32 vcc, 0, v82
	v_pk_fma_f32 v[80:81], v[98:99], v[80:81], s[10:11] op_sel_hi:[1,1,0]
	v_pk_fma_f32 v[72:73], v[108:109], v[46:47], v[72:73] op_sel_hi:[1,0,1] neg_lo:[1,0,0] neg_hi:[1,0,0]
	v_pk_mul_f32 v[80:81], v[98:99], v[80:81]
	v_pk_fma_f32 v[72:73], v[46:47], v[72:73], v[104:105] op_sel:[1,0,0]
	v_pk_mul_f32 v[80:81], v[84:85], v[80:81]
	v_cvt_pk_f16_f32 v92, v125, v126
	v_pk_mul_f32 v[84:85], v[82:83], v[80:81]
	v_pk_fma_f32 v[80:81], v[82:83], v[80:81], v[82:83] neg_lo:[1,0,0] neg_hi:[1,0,0]
	v_pk_fma_f32 v[74:75], v[90:91], v[46:47], v[74:75] op_sel_hi:[1,0,1]
	v_cndmask_b32_e32 v82, v80, v84, vcc
	v_cmp_gt_f32_e32 vcc, 0, v83
	v_and_b32_e32 v83, 0x7fffffff, v77
	v_cvt_pk_f16_f32 v80, v94, v95
	v_cndmask_b32_e32 v81, v81, v85, vcc
	v_cvt_pk_f16_f32 v81, v82, v81
	v_and_b32_e32 v82, 0x7fffffff, v76
	v_pk_fma_f32 v[82:83], v[82:83], s[8:9], 1.0 op_sel_hi:[1,0,0]
	v_add_u32_e32 v94, 0x1800, v121
	v_rcp_f32_e32 v82, v82
	v_rcp_f32_e32 v83, v83
	v_pk_mul_f32 v[84:85], v[76:77], v[76:77]
	ds_write2_b64 v94, v[96:97], v[80:81] offset0:32 offset1:36
	v_pk_mul_f32 v[84:85], v[84:85], s[16:17] op_sel_hi:[1,0]
	v_pk_fma_f32 v[80:81], v[82:83], s[0:1], v[122:123] op_sel_hi:[1,0,0]
	v_exp_f32_e32 v84, v84
	v_pk_fma_f32 v[80:81], v[82:83], v[80:81], s[14:15] op_sel_hi:[1,1,0]
	v_exp_f32_e32 v85, v85
	v_pk_fma_f32 v[80:81], v[82:83], v[80:81], s[6:7] op_sel_hi:[1,1,0]
	v_pk_mul_f32 v[96:97], v[78:79], v[78:79]
	v_pk_fma_f32 v[80:81], v[82:83], v[80:81], s[10:11] op_sel_hi:[1,1,0]
	v_cmp_gt_f32_e32 vcc, 0, v76
	v_pk_mul_f32 v[80:81], v[82:83], v[80:81]
	v_pk_mul_f32 v[96:97], v[96:97], s[16:17] op_sel_hi:[1,0]
	v_pk_mul_f32 v[80:81], v[84:85], v[80:81]
	global_load_dwordx4 v[84:87], v124, s[18:19] offset:128
	v_pk_mul_f32 v[98:99], v[76:77], v[80:81]
	v_pk_fma_f32 v[100:101], v[76:77], v[80:81], v[76:77] neg_lo:[1,0,0] neg_hi:[1,0,0]
	v_and_b32_e32 v81, 0x7fffffff, v79
	v_and_b32_e32 v80, 0x7fffffff, v78
	v_pk_fma_f32 v[102:103], v[80:81], s[8:9], 1.0 op_sel_hi:[1,0,0]
	global_load_dwordx4 v[80:83], v124, s[20:21] offset:128
	v_rcp_f32_e32 v102, v102
	v_rcp_f32_e32 v103, v103
	v_cndmask_b32_e32 v95, v100, v98, vcc
	v_cmp_gt_f32_e32 vcc, 0, v77
	v_exp_f32_e32 v96, v96
	v_pk_fma_f32 v[76:77], v[102:103], s[0:1], v[122:123] op_sel_hi:[1,0,0]
	v_exp_f32_e32 v97, v97
	v_pk_fma_f32 v[76:77], v[102:103], v[76:77], s[14:15] op_sel_hi:[1,1,0]
	v_cndmask_b32_e32 v98, v101, v99, vcc
	v_pk_fma_f32 v[76:77], v[102:103], v[76:77], s[6:7] op_sel_hi:[1,1,0]
	v_cmp_gt_f32_e32 vcc, 0, v78
	v_pk_fma_f32 v[76:77], v[102:103], v[76:77], s[10:11] op_sel_hi:[1,1,0]
	v_pk_mul_f32 v[90:91], v[72:73], v[72:73]
	v_pk_mul_f32 v[76:77], v[102:103], v[76:77]
	v_pk_mul_f32 v[90:91], v[90:91], s[16:17] op_sel_hi:[1,0]
	v_pk_mul_f32 v[76:77], v[96:97], v[76:77]
	v_pk_fma_f32 v[74:75], v[46:47], v[74:75], v[106:107] op_sel:[1,0,0]
	v_pk_mul_f32 v[96:97], v[78:79], v[76:77]
	v_pk_fma_f32 v[76:77], v[78:79], v[76:77], v[78:79] neg_lo:[1,0,0] neg_hi:[1,0,0]
	v_exp_f32_e32 v90, v90
	v_cndmask_b32_e32 v78, v76, v96, vcc
	v_cmp_gt_f32_e32 vcc, 0, v79
	v_and_b32_e32 v79, 0x7fffffff, v73
	v_cvt_pk_f16_f32 v76, v95, v98
	v_cndmask_b32_e32 v77, v77, v97, vcc
	v_cvt_pk_f16_f32 v77, v78, v77
	v_and_b32_e32 v78, 0x7fffffff, v72
	v_pk_fma_f32 v[78:79], v[78:79], s[8:9], 1.0 op_sel_hi:[1,0,0]
	v_add_u32_e32 v95, 0x3000, v121
	v_rcp_f32_e32 v78, v78
	v_rcp_f32_e32 v79, v79
	ds_write2_b64 v95, v[92:93], v[76:77] offset0:64 offset1:68
	v_exp_f32_e32 v91, v91
	v_and_b32_e32 v93, 0x7fffffff, v75
	v_pk_fma_f32 v[76:77], v[78:79], s[0:1], v[122:123] op_sel_hi:[1,0,0]
	v_and_b32_e32 v92, 0x7fffffff, v74
	v_pk_fma_f32 v[76:77], v[78:79], v[76:77], s[14:15] op_sel_hi:[1,1,0]
	v_pk_fma_f32 v[92:93], v[92:93], s[8:9], 1.0 op_sel_hi:[1,0,0]
	v_pk_fma_f32 v[76:77], v[78:79], v[76:77], s[6:7] op_sel_hi:[1,1,0]
	v_rcp_f32_e32 v92, v92
	v_pk_fma_f32 v[76:77], v[78:79], v[76:77], s[10:11] op_sel_hi:[1,1,0]
	v_rcp_f32_e32 v93, v93
	v_pk_mul_f32 v[76:77], v[78:79], v[76:77]
	v_cmp_gt_f32_e32 vcc, 0, v72
	v_pk_mul_f32 v[76:77], v[90:91], v[76:77]
	v_pk_mul_f32 v[78:79], v[74:75], v[74:75]
	v_pk_mul_f32 v[90:91], v[72:73], v[76:77]
	v_pk_fma_f32 v[76:77], v[72:73], v[76:77], v[72:73] neg_lo:[1,0,0] neg_hi:[1,0,0]
	s_nop 0
	v_cndmask_b32_e32 v90, v76, v90, vcc
	v_cmp_gt_f32_e32 vcc, 0, v73
	v_pk_fma_f32 v[72:73], v[92:93], s[0:1], v[122:123] op_sel_hi:[1,0,0]
	s_nop 0
	v_cndmask_b32_e32 v91, v77, v91, vcc
	v_pk_mul_f32 v[76:77], v[78:79], s[16:17] op_sel_hi:[1,0]
	v_pk_fma_f32 v[72:73], v[92:93], v[72:73], s[14:15] op_sel_hi:[1,1,0]
	v_exp_f32_e32 v76, v76
	v_exp_f32_e32 v77, v77
	v_pk_fma_f32 v[72:73], v[92:93], v[72:73], s[6:7] op_sel_hi:[1,1,0]
	v_cmp_gt_f32_e32 vcc, 0, v74
	v_pk_fma_f32 v[72:73], v[92:93], v[72:73], s[10:11] op_sel_hi:[1,1,0]
	s_nop 0
	v_pk_mul_f32 v[72:73], v[92:93], v[72:73]
	s_nop 0
	v_pk_mul_f32 v[72:73], v[76:77], v[72:73]
	s_nop 0
	v_pk_mul_f32 v[76:77], v[74:75], v[72:73]
	v_pk_fma_f32 v[72:73], v[74:75], v[72:73], v[74:75] neg_lo:[1,0,0] neg_hi:[1,0,0]
	s_nop 0
	v_cndmask_b32_e32 v74, v72, v76, vcc
	v_cmp_gt_f32_e32 vcc, 0, v75
	v_cvt_pk_f16_f32 v72, v90, v91
	v_add_u32_e32 v90, 0x4800, v121
	v_cndmask_b32_e32 v73, v73, v77, vcc
	v_cvt_pk_f16_f32 v73, v74, v73
	global_load_dwordx4 v[76:79], v124, s[18:19] offset:192
	s_waitcnt vmcnt(2)
	v_pk_fma_f32 v[68:69], v[84:85], v[60:61], v[68:69] op_sel_hi:[1,0,1] neg_lo:[1,0,0] neg_hi:[1,0,0]
	ds_write2_b64 v90, v[88:89], v[72:73] offset0:96 offset1:100
	global_load_dwordx4 v[72:75], v124, s[20:21] offset:192
	s_waitcnt vmcnt(2)
	v_pk_fma_f32 v[68:69], v[60:61], v[68:69], v[80:81] op_sel:[1,0,0]
	v_xor_b32_e32 v87, 0x80000000, v87
	v_and_b32_e32 v89, 0x7fffffff, v69
	v_and_b32_e32 v88, 0x7fffffff, v68
	v_pk_fma_f32 v[88:89], v[88:89], s[8:9], 1.0 op_sel_hi:[1,0,0]
	v_xor_b32_e32 v86, 0x80000000, v86
	v_rcp_f32_e32 v88, v88
	v_rcp_f32_e32 v89, v89
	v_pk_mul_f32 v[96:97], v[68:69], v[68:69]
	v_pk_fma_f32 v[70:71], v[86:87], v[60:61], v[70:71] op_sel_hi:[1,0,1]
	v_pk_mul_f32 v[96:97], v[96:97], s[16:17] op_sel_hi:[1,0]
	v_pk_fma_f32 v[92:93], v[88:89], s[0:1], v[122:123] op_sel_hi:[1,0,0]
	v_pk_fma_f32 v[70:71], v[60:61], v[70:71], v[82:83] op_sel:[1,0,0]
	v_pk_fma_f32 v[92:93], v[88:89], v[92:93], s[14:15] op_sel_hi:[1,1,0]
	v_exp_f32_e32 v96, v96
	v_exp_f32_e32 v97, v97
	v_pk_fma_f32 v[92:93], v[88:89], v[92:93], s[6:7] op_sel_hi:[1,1,0]
	v_and_b32_e32 v99, 0x7fffffff, v71
	v_and_b32_e32 v98, 0x7fffffff, v70
	v_pk_fma_f32 v[92:93], v[88:89], v[92:93], s[10:11] op_sel_hi:[1,1,0]
	v_pk_fma_f32 v[98:99], v[98:99], s[8:9], 1.0 op_sel_hi:[1,0,0]
	v_pk_mul_f32 v[88:89], v[88:89], v[92:93]
	v_rcp_f32_e32 v98, v98
	v_rcp_f32_e32 v99, v99
	v_pk_mul_f32 v[88:89], v[96:97], v[88:89]
	v_cmp_gt_f32_e32 vcc, 0, v68
	v_pk_mul_f32 v[96:97], v[68:69], v[88:89]
	v_pk_fma_f32 v[88:89], v[68:69], v[88:89], v[68:69] neg_lo:[1,0,0] neg_hi:[1,0,0]
	v_pk_mul_f32 v[92:93], v[70:71], v[70:71]
	v_cndmask_b32_e32 v91, v88, v96, vcc
	v_cmp_gt_f32_e32 vcc, 0, v69
	v_pk_fma_f32 v[68:69], v[98:99], s[0:1], v[122:123] op_sel_hi:[1,0,0]
	v_pk_fma_f32 v[64:65], v[84:85], v[62:63], v[64:65] op_sel_hi:[1,0,1] neg_lo:[1,0,0] neg_hi:[1,0,0]
	v_cndmask_b32_e32 v96, v89, v97, vcc
	v_pk_mul_f32 v[88:89], v[92:93], s[16:17] op_sel_hi:[1,0]
	v_pk_fma_f32 v[68:69], v[98:99], v[68:69], s[14:15] op_sel_hi:[1,1,0]
	v_exp_f32_e32 v88, v88
	v_exp_f32_e32 v89, v89
	v_pk_fma_f32 v[68:69], v[98:99], v[68:69], s[6:7] op_sel_hi:[1,1,0]
	v_cmp_gt_f32_e32 vcc, 0, v70
	v_pk_fma_f32 v[68:69], v[98:99], v[68:69], s[10:11] op_sel_hi:[1,1,0]
	v_pk_fma_f32 v[64:65], v[62:63], v[64:65], v[80:81] op_sel:[1,0,0]
	v_pk_mul_f32 v[68:69], v[98:99], v[68:69]
	v_pk_mul_f32 v[92:93], v[64:65], v[64:65]
	v_pk_mul_f32 v[68:69], v[88:89], v[68:69]
	v_pk_fma_f32 v[66:67], v[86:87], v[62:63], v[66:67] op_sel_hi:[1,0,1]
	v_pk_mul_f32 v[88:89], v[70:71], v[68:69]
	v_pk_fma_f32 v[68:69], v[70:71], v[68:69], v[70:71] neg_lo:[1,0,0] neg_hi:[1,0,0]
	v_and_b32_e32 v70, 0x7fffffff, v64
	v_cndmask_b32_e32 v88, v68, v88, vcc
	v_cmp_gt_f32_e32 vcc, 0, v71
	v_and_b32_e32 v71, 0x7fffffff, v65
	v_pk_fma_f32 v[70:71], v[70:71], s[8:9], 1.0 op_sel_hi:[1,0,0]
	v_cndmask_b32_e32 v69, v69, v89, vcc
	v_rcp_f32_e32 v70, v70
	v_rcp_f32_e32 v71, v71
	v_cvt_pk_f16_f32 v69, v88, v69
	v_pk_mul_f32 v[92:93], v[92:93], s[16:17] op_sel_hi:[1,0]
	v_pk_fma_f32 v[66:67], v[62:63], v[66:67], v[82:83] op_sel:[1,0,0]
	v_pk_fma_f32 v[88:89], v[70:71], s[0:1], v[122:123] op_sel_hi:[1,0,0]
	v_exp_f32_e32 v92, v92
	v_pk_fma_f32 v[88:89], v[70:71], v[88:89], s[14:15] op_sel_hi:[1,1,0]
	v_exp_f32_e32 v93, v93
	v_cvt_pk_f16_f32 v68, v91, v96
	v_pk_fma_f32 v[88:89], v[70:71], v[88:89], s[6:7] op_sel_hi:[1,1,0]
	v_and_b32_e32 v97, 0x7fffffff, v67
	v_and_b32_e32 v96, 0x7fffffff, v66
	v_pk_fma_f32 v[88:89], v[70:71], v[88:89], s[10:11] op_sel_hi:[1,1,0]
	v_pk_fma_f32 v[96:97], v[96:97], s[8:9], 1.0 op_sel_hi:[1,0,0]
	v_pk_mul_f32 v[70:71], v[70:71], v[88:89]
	v_rcp_f32_e32 v96, v96
	v_rcp_f32_e32 v97, v97
	v_pk_mul_f32 v[70:71], v[92:93], v[70:71]
	v_cmp_gt_f32_e32 vcc, 0, v64
	v_pk_mul_f32 v[92:93], v[64:65], v[70:71]
	v_pk_fma_f32 v[70:71], v[64:65], v[70:71], v[64:65] neg_lo:[1,0,0] neg_hi:[1,0,0]
	v_pk_mul_f32 v[88:89], v[66:67], v[66:67]
	v_cndmask_b32_e32 v91, v70, v92, vcc
	v_cmp_gt_f32_e32 vcc, 0, v65
	v_pk_fma_f32 v[64:65], v[96:97], s[0:1], v[122:123] op_sel_hi:[1,0,0]
	v_pk_fma_f32 v[56:57], v[84:85], v[44:45], v[56:57] op_sel_hi:[1,0,1] neg_lo:[1,0,0] neg_hi:[1,0,0]
	v_cndmask_b32_e32 v92, v71, v93, vcc
	v_pk_mul_f32 v[70:71], v[88:89], s[16:17] op_sel_hi:[1,0]
	v_pk_fma_f32 v[64:65], v[96:97], v[64:65], s[14:15] op_sel_hi:[1,1,0]
	v_exp_f32_e32 v70, v70
	v_exp_f32_e32 v71, v71
	v_pk_fma_f32 v[64:65], v[96:97], v[64:65], s[6:7] op_sel_hi:[1,1,0]
	v_cmp_gt_f32_e32 vcc, 0, v66
	v_pk_fma_f32 v[64:65], v[96:97], v[64:65], s[10:11] op_sel_hi:[1,1,0]
	v_pk_fma_f32 v[56:57], v[44:45], v[56:57], v[80:81] op_sel:[1,0,0]
	v_pk_mul_f32 v[64:65], v[96:97], v[64:65]
	v_pk_mul_f32 v[88:89], v[56:57], v[56:57]
	v_pk_mul_f32 v[64:65], v[70:71], v[64:65]
	v_pk_fma_f32 v[58:59], v[86:87], v[44:45], v[58:59] op_sel_hi:[1,0,1]
	v_pk_mul_f32 v[70:71], v[66:67], v[64:65]
	v_pk_fma_f32 v[64:65], v[66:67], v[64:65], v[66:67] neg_lo:[1,0,0] neg_hi:[1,0,0]
	v_and_b32_e32 v66, 0x7fffffff, v56
	v_cndmask_b32_e32 v70, v64, v70, vcc
	v_cmp_gt_f32_e32 vcc, 0, v67
	v_and_b32_e32 v67, 0x7fffffff, v57
	v_pk_fma_f32 v[66:67], v[66:67], s[8:9], 1.0 op_sel_hi:[1,0,0]
	v_cndmask_b32_e32 v65, v65, v71, vcc
	v_rcp_f32_e32 v66, v66
	v_rcp_f32_e32 v67, v67
	v_cvt_pk_f16_f32 v65, v70, v65
	v_pk_mul_f32 v[88:89], v[88:89], s[16:17] op_sel_hi:[1,0]
	v_pk_fma_f32 v[58:59], v[44:45], v[58:59], v[82:83] op_sel:[1,0,0]
	v_pk_fma_f32 v[70:71], v[66:67], s[0:1], v[122:123] op_sel_hi:[1,0,0]
	v_exp_f32_e32 v88, v88
	v_pk_fma_f32 v[70:71], v[66:67], v[70:71], s[14:15] op_sel_hi:[1,1,0]
	v_exp_f32_e32 v89, v89
	v_cvt_pk_f16_f32 v64, v91, v92
	v_pk_fma_f32 v[70:71], v[66:67], v[70:71], s[6:7] op_sel_hi:[1,1,0]
	v_and_b32_e32 v93, 0x7fffffff, v59
	v_and_b32_e32 v92, 0x7fffffff, v58
	v_pk_fma_f32 v[70:71], v[66:67], v[70:71], s[10:11] op_sel_hi:[1,1,0]
	v_pk_fma_f32 v[92:93], v[92:93], s[8:9], 1.0 op_sel_hi:[1,0,0]
	v_pk_mul_f32 v[66:67], v[66:67], v[70:71]
	v_rcp_f32_e32 v92, v92
	v_rcp_f32_e32 v93, v93
	v_pk_mul_f32 v[66:67], v[88:89], v[66:67]
	v_cmp_gt_f32_e32 vcc, 0, v56
	v_pk_mul_f32 v[88:89], v[56:57], v[66:67]
	v_pk_fma_f32 v[66:67], v[56:57], v[66:67], v[56:57] neg_lo:[1,0,0] neg_hi:[1,0,0]
	v_pk_mul_f32 v[70:71], v[58:59], v[58:59]
	v_cndmask_b32_e32 v88, v66, v88, vcc
	v_cmp_gt_f32_e32 vcc, 0, v57
	v_pk_fma_f32 v[56:57], v[92:93], s[0:1], v[122:123] op_sel_hi:[1,0,0]
	v_pk_fma_f32 v[52:53], v[84:85], v[46:47], v[52:53] op_sel_hi:[1,0,1] neg_lo:[1,0,0] neg_hi:[1,0,0]
	v_cndmask_b32_e32 v89, v67, v89, vcc
	v_pk_mul_f32 v[66:67], v[70:71], s[16:17] op_sel_hi:[1,0]
	v_pk_fma_f32 v[56:57], v[92:93], v[56:57], s[14:15] op_sel_hi:[1,1,0]
	v_exp_f32_e32 v66, v66
	v_exp_f32_e32 v67, v67
	v_pk_fma_f32 v[56:57], v[92:93], v[56:57], s[6:7] op_sel_hi:[1,1,0]
	v_cmp_gt_f32_e32 vcc, 0, v58
	v_pk_fma_f32 v[56:57], v[92:93], v[56:57], s[10:11] op_sel_hi:[1,1,0]
	v_pk_fma_f32 v[52:53], v[46:47], v[52:53], v[80:81] op_sel:[1,0,0]
	v_pk_mul_f32 v[56:57], v[92:93], v[56:57]
	v_pk_mul_f32 v[70:71], v[52:53], v[52:53]
	v_pk_mul_f32 v[56:57], v[66:67], v[56:57]
	v_pk_fma_f32 v[54:55], v[86:87], v[46:47], v[54:55] op_sel_hi:[1,0,1]
	v_pk_mul_f32 v[66:67], v[58:59], v[56:57]
	v_pk_fma_f32 v[56:57], v[58:59], v[56:57], v[58:59] neg_lo:[1,0,0] neg_hi:[1,0,0]
	v_and_b32_e32 v58, 0x7fffffff, v52
	v_cndmask_b32_e32 v66, v56, v66, vcc
	v_cmp_gt_f32_e32 vcc, 0, v59
	v_and_b32_e32 v59, 0x7fffffff, v53
	v_pk_fma_f32 v[58:59], v[58:59], s[8:9], 1.0 op_sel_hi:[1,0,0]
	v_cndmask_b32_e32 v57, v57, v67, vcc
	v_rcp_f32_e32 v58, v58
	v_rcp_f32_e32 v59, v59
	v_cvt_pk_f16_f32 v57, v66, v57
	v_pk_mul_f32 v[70:71], v[70:71], s[16:17] op_sel_hi:[1,0]
	v_pk_fma_f32 v[54:55], v[46:47], v[54:55], v[82:83] op_sel:[1,0,0]
	v_pk_fma_f32 v[66:67], v[58:59], s[0:1], v[122:123] op_sel_hi:[1,0,0]
	v_exp_f32_e32 v70, v70
	v_pk_fma_f32 v[66:67], v[58:59], v[66:67], s[14:15] op_sel_hi:[1,1,0]
	v_exp_f32_e32 v71, v71
	v_pk_fma_f32 v[66:67], v[58:59], v[66:67], s[6:7] op_sel_hi:[1,1,0]
	v_and_b32_e32 v81, 0x7fffffff, v55
	v_and_b32_e32 v80, 0x7fffffff, v54
	v_pk_fma_f32 v[66:67], v[58:59], v[66:67], s[10:11] op_sel_hi:[1,1,0]
	v_pk_fma_f32 v[80:81], v[80:81], s[8:9], 1.0 op_sel_hi:[1,0,0]
	v_pk_mul_f32 v[58:59], v[58:59], v[66:67]
	v_rcp_f32_e32 v80, v80
	v_rcp_f32_e32 v81, v81
	v_pk_mul_f32 v[58:59], v[70:71], v[58:59]
	v_cmp_gt_f32_e32 vcc, 0, v52
	v_pk_mul_f32 v[70:71], v[52:53], v[58:59]
	v_pk_fma_f32 v[58:59], v[52:53], v[58:59], v[52:53] neg_lo:[1,0,0] neg_hi:[1,0,0]
	v_pk_mul_f32 v[66:67], v[54:55], v[54:55]
	v_cndmask_b32_e32 v70, v58, v70, vcc
	v_cmp_gt_f32_e32 vcc, 0, v53
	v_pk_fma_f32 v[52:53], v[80:81], s[0:1], v[122:123] op_sel_hi:[1,0,0]
	s_waitcnt vmcnt(1)
	v_pk_fma_f32 v[40:41], v[76:77], v[62:63], v[40:41] op_sel_hi:[1,0,1] neg_lo:[1,0,0] neg_hi:[1,0,0]
	v_cndmask_b32_e32 v71, v59, v71, vcc
	v_pk_mul_f32 v[58:59], v[66:67], s[16:17] op_sel_hi:[1,0]
	v_pk_fma_f32 v[52:53], v[80:81], v[52:53], s[14:15] op_sel_hi:[1,1,0]
	v_exp_f32_e32 v58, v58
	v_exp_f32_e32 v59, v59
	v_pk_fma_f32 v[52:53], v[80:81], v[52:53], s[6:7] op_sel_hi:[1,1,0]
	v_cmp_gt_f32_e32 vcc, 0, v54
	v_pk_fma_f32 v[52:53], v[80:81], v[52:53], s[10:11] op_sel_hi:[1,1,0]
	s_waitcnt vmcnt(0)
	v_pk_fma_f32 v[40:41], v[62:63], v[40:41], v[72:73] op_sel:[1,0,0]
	v_pk_mul_f32 v[52:53], v[80:81], v[52:53]
	v_pk_fma_f32 v[36:37], v[76:77], v[44:45], v[36:37] op_sel_hi:[1,0,1] neg_lo:[1,0,0] neg_hi:[1,0,0]
	v_pk_mul_f32 v[52:53], v[58:59], v[52:53]
	v_pk_fma_f32 v[32:33], v[76:77], v[46:47], v[32:33] op_sel_hi:[1,0,1] neg_lo:[1,0,0] neg_hi:[1,0,0]
	v_pk_mul_f32 v[58:59], v[54:55], v[52:53]
	v_pk_fma_f32 v[52:53], v[54:55], v[52:53], v[54:55] neg_lo:[1,0,0] neg_hi:[1,0,0]
	v_pk_fma_f32 v[32:33], v[46:47], v[32:33], v[72:73] op_sel:[1,0,0]
	v_cndmask_b32_e32 v54, v52, v58, vcc
	v_cmp_gt_f32_e32 vcc, 0, v55
	v_cvt_pk_f16_f32 v52, v70, v71
	v_cvt_pk_f16_f32 v56, v88, v89
	v_cndmask_b32_e32 v53, v53, v59, vcc
	v_cvt_pk_f16_f32 v53, v54, v53
	v_pk_fma_f32 v[54:55], v[76:77], v[60:61], v[48:49] op_sel_hi:[1,0,1] neg_lo:[1,0,0] neg_hi:[1,0,0]
	v_xor_b32_e32 v49, 0x80000000, v79
	v_pk_fma_f32 v[54:55], v[60:61], v[54:55], v[72:73] op_sel:[1,0,0]
	v_xor_b32_e32 v48, 0x80000000, v78
	v_and_b32_e32 v59, 0x7fffffff, v55
	v_and_b32_e32 v58, 0x7fffffff, v54
	v_pk_fma_f32 v[58:59], v[58:59], s[8:9], 1.0 op_sel_hi:[1,0,0]
	v_pk_mul_f32 v[70:71], v[54:55], v[54:55]
	v_rcp_f32_e32 v58, v58
	v_rcp_f32_e32 v59, v59
	v_pk_fma_f32 v[50:51], v[48:49], v[60:61], v[50:51] op_sel_hi:[1,0,1]
	v_pk_mul_f32 v[70:71], v[70:71], s[16:17] op_sel_hi:[1,0]
	v_pk_fma_f32 v[50:51], v[60:61], v[50:51], v[74:75] op_sel:[1,0,0]
	v_pk_fma_f32 v[66:67], v[58:59], s[0:1], v[122:123] op_sel_hi:[1,0,0]
	v_exp_f32_e32 v70, v70
	v_pk_fma_f32 v[66:67], v[58:59], v[66:67], s[14:15] op_sel_hi:[1,1,0]
	v_exp_f32_e32 v71, v71
	v_pk_fma_f32 v[66:67], v[58:59], v[66:67], s[6:7] op_sel_hi:[1,1,0]
	v_and_b32_e32 v79, 0x7fffffff, v51
	v_and_b32_e32 v78, 0x7fffffff, v50
	v_pk_fma_f32 v[66:67], v[58:59], v[66:67], s[10:11] op_sel_hi:[1,1,0]
	v_pk_fma_f32 v[78:79], v[78:79], s[8:9], 1.0 op_sel_hi:[1,0,0]
	v_pk_mul_f32 v[58:59], v[58:59], v[66:67]
	v_rcp_f32_e32 v78, v78
	v_rcp_f32_e32 v79, v79
	v_pk_mul_f32 v[58:59], v[70:71], v[58:59]
	v_cmp_gt_f32_e32 vcc, 0, v54
	v_pk_mul_f32 v[70:71], v[54:55], v[58:59]
	v_pk_fma_f32 v[58:59], v[54:55], v[58:59], v[54:55] neg_lo:[1,0,0] neg_hi:[1,0,0]
	v_pk_mul_f32 v[66:67], v[50:51], v[50:51]
	v_cndmask_b32_e32 v70, v58, v70, vcc
	v_cmp_gt_f32_e32 vcc, 0, v55
	v_pk_fma_f32 v[54:55], v[78:79], s[0:1], v[122:123] op_sel_hi:[1,0,0]
	v_pk_fma_f32 v[42:43], v[48:49], v[62:63], v[42:43] op_sel_hi:[1,0,1]
	v_cndmask_b32_e32 v71, v59, v71, vcc
	v_pk_mul_f32 v[58:59], v[66:67], s[16:17] op_sel_hi:[1,0]
	v_pk_fma_f32 v[54:55], v[78:79], v[54:55], s[14:15] op_sel_hi:[1,1,0]
	v_exp_f32_e32 v58, v58
	v_exp_f32_e32 v59, v59
	v_pk_fma_f32 v[54:55], v[78:79], v[54:55], s[6:7] op_sel_hi:[1,1,0]
	v_cmp_gt_f32_e32 vcc, 0, v50
	v_pk_fma_f32 v[54:55], v[78:79], v[54:55], s[10:11] op_sel_hi:[1,1,0]
	v_pk_fma_f32 v[42:43], v[62:63], v[42:43], v[74:75] op_sel:[1,0,0]
	v_pk_mul_f32 v[54:55], v[78:79], v[54:55]
	v_and_b32_e32 v67, 0x7fffffff, v43
	v_pk_mul_f32 v[54:55], v[58:59], v[54:55]
	v_and_b32_e32 v66, 0x7fffffff, v42
	v_pk_mul_f32 v[58:59], v[50:51], v[54:55]
	v_pk_fma_f32 v[54:55], v[50:51], v[54:55], v[50:51] neg_lo:[1,0,0] neg_hi:[1,0,0]
	v_cvt_pk_f16_f32 v50, v70, v71
	v_cndmask_b32_e32 v54, v54, v58, vcc
	v_cmp_gt_f32_e32 vcc, 0, v51
	v_pk_fma_f32 v[66:67], v[66:67], s[8:9], 1.0 op_sel_hi:[1,0,0]
	v_pk_fma_f32 v[38:39], v[48:49], v[44:45], v[38:39] op_sel_hi:[1,0,1]
	v_cndmask_b32_e32 v51, v55, v59, vcc
	v_cvt_pk_f16_f32 v51, v54, v51
	v_and_b32_e32 v55, 0x7fffffff, v41
	v_and_b32_e32 v54, 0x7fffffff, v40
	v_pk_fma_f32 v[54:55], v[54:55], s[8:9], 1.0 op_sel_hi:[1,0,0]
	v_pk_mul_f32 v[58:59], v[40:41], v[40:41]
	v_rcp_f32_e32 v54, v54
	v_rcp_f32_e32 v55, v55
	ds_write2_b64 v121, v[68:69], v[50:51] offset0:8 offset1:12
	v_pk_mul_f32 v[58:59], v[58:59], s[16:17] op_sel_hi:[1,0]
	v_rcp_f32_e32 v66, v66
	v_pk_fma_f32 v[50:51], v[54:55], s[0:1], v[122:123] op_sel_hi:[1,0,0]
	v_exp_f32_e32 v58, v58
	v_pk_fma_f32 v[50:51], v[54:55], v[50:51], s[14:15] op_sel_hi:[1,1,0]
	v_exp_f32_e32 v59, v59
	v_pk_fma_f32 v[50:51], v[54:55], v[50:51], s[6:7] op_sel_hi:[1,1,0]
	v_rcp_f32_e32 v67, v67
	v_pk_fma_f32 v[50:51], v[54:55], v[50:51], s[10:11] op_sel_hi:[1,1,0]
	v_cmp_gt_f32_e32 vcc, 0, v40
	v_pk_mul_f32 v[50:51], v[54:55], v[50:51]
	v_pk_mul_f32 v[54:55], v[42:43], v[42:43]
	v_pk_mul_f32 v[50:51], v[58:59], v[50:51]
	v_pk_fma_f32 v[34:35], v[48:49], v[46:47], v[34:35] op_sel_hi:[1,0,1]
	v_pk_mul_f32 v[58:59], v[40:41], v[50:51]
	v_pk_fma_f32 v[50:51], v[40:41], v[50:51], v[40:41] neg_lo:[1,0,0] neg_hi:[1,0,0]
	v_pk_fma_f32 v[34:35], v[46:47], v[34:35], v[74:75] op_sel:[1,0,0]
	v_cndmask_b32_e32 v58, v50, v58, vcc
	v_cmp_gt_f32_e32 vcc, 0, v41
	v_pk_fma_f32 v[40:41], v[66:67], s[0:1], v[122:123] op_sel_hi:[1,0,0]
	s_nop 0
	v_cndmask_b32_e32 v59, v51, v59, vcc
	v_pk_mul_f32 v[50:51], v[54:55], s[16:17] op_sel_hi:[1,0]
	v_pk_fma_f32 v[40:41], v[66:67], v[40:41], s[14:15] op_sel_hi:[1,1,0]
	v_exp_f32_e32 v50, v50
	v_exp_f32_e32 v51, v51
	v_pk_fma_f32 v[40:41], v[66:67], v[40:41], s[6:7] op_sel_hi:[1,1,0]
	v_cmp_gt_f32_e32 vcc, 0, v42
	v_pk_fma_f32 v[40:41], v[66:67], v[40:41], s[10:11] op_sel_hi:[1,1,0]
	v_pk_fma_f32 v[54:55], v[44:45], v[38:39], v[74:75] op_sel:[1,0,0]
	v_pk_mul_f32 v[40:41], v[66:67], v[40:41]
	v_and_b32_e32 v69, 0x7fffffff, v55
	v_pk_mul_f32 v[40:41], v[50:51], v[40:41]
	v_and_b32_e32 v68, 0x7fffffff, v54
	v_pk_mul_f32 v[50:51], v[42:43], v[40:41]
	v_pk_fma_f32 v[40:41], v[42:43], v[40:41], v[42:43] neg_lo:[1,0,0] neg_hi:[1,0,0]
	v_pk_fma_f32 v[68:69], v[68:69], s[8:9], 1.0 op_sel_hi:[1,0,0]
	v_cndmask_b32_e32 v42, v40, v50, vcc
	v_cmp_gt_f32_e32 vcc, 0, v43
	v_cvt_pk_f16_f32 v40, v58, v59
	v_rcp_f32_e32 v68, v68
	v_cndmask_b32_e32 v41, v41, v51, vcc
	v_pk_fma_f32 v[50:51], v[44:45], v[36:37], v[72:73] op_sel:[1,0,0]
	v_cvt_pk_f16_f32 v41, v42, v41
	v_and_b32_e32 v37, 0x7fffffff, v51
	v_and_b32_e32 v36, 0x7fffffff, v50
	v_pk_fma_f32 v[36:37], v[36:37], s[8:9], 1.0 op_sel_hi:[1,0,0]
	ds_write2_b64 v94, v[64:65], v[40:41] offset0:40 offset1:44
	v_rcp_f32_e32 v36, v36
	v_rcp_f32_e32 v37, v37
	v_pk_mul_f32 v[40:41], v[50:51], v[50:51]
	v_rcp_f32_e32 v69, v69
	v_pk_mul_f32 v[40:41], v[40:41], s[16:17] op_sel_hi:[1,0]
	v_pk_fma_f32 v[38:39], v[36:37], s[0:1], v[122:123] op_sel_hi:[1,0,0]
	v_exp_f32_e32 v40, v40
	v_pk_fma_f32 v[38:39], v[36:37], v[38:39], s[14:15] op_sel_hi:[1,1,0]
	v_exp_f32_e32 v41, v41
	v_pk_fma_f32 v[38:39], v[36:37], v[38:39], s[6:7] op_sel_hi:[1,1,0]
	v_pk_mul_f32 v[58:59], v[54:55], v[54:55]
	v_pk_fma_f32 v[38:39], v[36:37], v[38:39], s[10:11] op_sel_hi:[1,1,0]
	v_cmp_gt_f32_e32 vcc, 0, v50
	v_pk_mul_f32 v[36:37], v[36:37], v[38:39]
	v_pk_mul_f32 v[58:59], v[58:59], s[16:17] op_sel_hi:[1,0]
	v_pk_mul_f32 v[36:37], v[40:41], v[36:37]
	global_load_dwordx4 v[40:43], v124, s[18:19] offset:256
	v_pk_mul_f32 v[64:65], v[50:51], v[36:37]
	v_pk_fma_f32 v[66:67], v[50:51], v[36:37], v[50:51] neg_lo:[1,0,0] neg_hi:[1,0,0]
	global_load_dwordx4 v[36:39], v124, s[20:21] offset:256
	v_cndmask_b32_e32 v64, v66, v64, vcc
	v_cmp_gt_f32_e32 vcc, 0, v51
	v_pk_fma_f32 v[50:51], v[68:69], s[0:1], v[122:123] op_sel_hi:[1,0,0]
	v_exp_f32_e32 v58, v58
	v_pk_fma_f32 v[50:51], v[68:69], v[50:51], s[14:15] op_sel_hi:[1,1,0]
	v_exp_f32_e32 v59, v59
	v_pk_fma_f32 v[50:51], v[68:69], v[50:51], s[6:7] op_sel_hi:[1,1,0]
	v_cndmask_b32_e32 v65, v67, v65, vcc
	v_pk_fma_f32 v[50:51], v[68:69], v[50:51], s[10:11] op_sel_hi:[1,1,0]
	v_cmp_gt_f32_e32 vcc, 0, v54
	v_pk_mul_f32 v[50:51], v[68:69], v[50:51]
	s_nop 0
	v_pk_mul_f32 v[50:51], v[58:59], v[50:51]
	s_nop 0
	v_pk_mul_f32 v[58:59], v[54:55], v[50:51]
	v_pk_fma_f32 v[50:51], v[54:55], v[50:51], v[54:55] neg_lo:[1,0,0] neg_hi:[1,0,0]
	s_nop 0
	v_cndmask_b32_e32 v54, v50, v58, vcc
	v_cmp_gt_f32_e32 vcc, 0, v55
	v_and_b32_e32 v55, 0x7fffffff, v33
	v_cvt_pk_f16_f32 v50, v64, v65
	v_cndmask_b32_e32 v51, v51, v59, vcc
	v_cvt_pk_f16_f32 v51, v54, v51
	v_and_b32_e32 v54, 0x7fffffff, v32
	v_pk_fma_f32 v[54:55], v[54:55], s[8:9], 1.0 op_sel_hi:[1,0,0]
	ds_write2_b64 v95, v[56:57], v[50:51] offset0:72 offset1:76
	v_rcp_f32_e32 v54, v54
	v_rcp_f32_e32 v55, v55
	v_pk_mul_f32 v[50:51], v[32:33], v[32:33]
	v_and_b32_e32 v57, 0x7fffffff, v35
	v_pk_mul_f32 v[50:51], v[50:51], s[16:17] op_sel_hi:[1,0]
	v_pk_fma_f32 v[48:49], v[54:55], s[0:1], v[122:123] op_sel_hi:[1,0,0]
	v_exp_f32_e32 v50, v50
	v_pk_fma_f32 v[48:49], v[54:55], v[48:49], s[14:15] op_sel_hi:[1,1,0]
	v_exp_f32_e32 v51, v51
	v_pk_fma_f32 v[48:49], v[54:55], v[48:49], s[6:7] op_sel_hi:[1,1,0]
	v_and_b32_e32 v56, 0x7fffffff, v34
	v_pk_fma_f32 v[48:49], v[54:55], v[48:49], s[10:11] op_sel_hi:[1,1,0]
	v_pk_fma_f32 v[56:57], v[56:57], s[8:9], 1.0 op_sel_hi:[1,0,0]
	v_pk_mul_f32 v[48:49], v[54:55], v[48:49]
	v_rcp_f32_e32 v56, v56
	v_rcp_f32_e32 v57, v57
	v_pk_mul_f32 v[48:49], v[50:51], v[48:49]
	v_cmp_gt_f32_e32 vcc, 0, v32
	v_pk_mul_f32 v[50:51], v[32:33], v[48:49]
	v_pk_fma_f32 v[48:49], v[32:33], v[48:49], v[32:33] neg_lo:[1,0,0] neg_hi:[1,0,0]
	v_pk_mul_f32 v[54:55], v[34:35], v[34:35]
	v_cndmask_b32_e32 v50, v48, v50, vcc
	v_cmp_gt_f32_e32 vcc, 0, v33
	v_pk_fma_f32 v[32:33], v[56:57], s[0:1], v[122:123] op_sel_hi:[1,0,0]
	s_nop 0
	v_cndmask_b32_e32 v51, v49, v51, vcc
	v_pk_mul_f32 v[48:49], v[54:55], s[16:17] op_sel_hi:[1,0]
	v_pk_fma_f32 v[32:33], v[56:57], v[32:33], s[14:15] op_sel_hi:[1,1,0]
	v_exp_f32_e32 v48, v48
	v_exp_f32_e32 v49, v49
	v_pk_fma_f32 v[32:33], v[56:57], v[32:33], s[6:7] op_sel_hi:[1,1,0]
	v_cmp_gt_f32_e32 vcc, 0, v34
	v_pk_fma_f32 v[32:33], v[56:57], v[32:33], s[10:11] op_sel_hi:[1,1,0]
	s_nop 0
	v_pk_mul_f32 v[32:33], v[56:57], v[32:33]
	s_nop 0
	v_pk_mul_f32 v[32:33], v[48:49], v[32:33]
	s_nop 0
	v_pk_mul_f32 v[48:49], v[34:35], v[32:33]
	v_pk_fma_f32 v[32:33], v[34:35], v[32:33], v[34:35] neg_lo:[1,0,0] neg_hi:[1,0,0]
	s_nop 0
	v_cndmask_b32_e32 v34, v32, v48, vcc
	v_cmp_gt_f32_e32 vcc, 0, v35
	v_cvt_pk_f16_f32 v32, v50, v51
	s_nop 0
	v_cndmask_b32_e32 v33, v33, v49, vcc
	v_cvt_pk_f16_f32 v33, v34, v33
	global_load_dwordx4 v[48:51], v124, s[18:19] offset:320
	ds_write2_b64 v90, v[52:53], v[32:33] offset0:104 offset1:108
	global_load_dwordx4 v[32:35], v124, s[20:21] offset:320
	s_waitcnt vmcnt(3)
	v_pk_fma_f32 v[28:29], v[40:41], v[60:61], v[28:29] op_sel_hi:[1,0,1] neg_lo:[1,0,0] neg_hi:[1,0,0]
	v_xor_b32_e32 v43, 0x80000000, v43
	v_xor_b32_e32 v42, 0x80000000, v42
	s_waitcnt vmcnt(2)
	v_pk_fma_f32 v[28:29], v[60:61], v[28:29], v[36:37] op_sel:[1,0,0]
	v_pk_fma_f32 v[30:31], v[42:43], v[60:61], v[30:31] op_sel_hi:[1,0,1]
	v_and_b32_e32 v53, 0x7fffffff, v29
	v_and_b32_e32 v52, 0x7fffffff, v28
	v_pk_fma_f32 v[52:53], v[52:53], s[8:9], 1.0 op_sel_hi:[1,0,0]
	v_pk_mul_f32 v[56:57], v[28:29], v[28:29]
	v_rcp_f32_e32 v52, v52
	v_rcp_f32_e32 v53, v53
	v_pk_mul_f32 v[56:57], v[56:57], s[16:17] op_sel_hi:[1,0]
	v_pk_fma_f32 v[30:31], v[60:61], v[30:31], v[38:39] op_sel:[1,0,0]
	v_exp_f32_e32 v56, v56
	v_pk_fma_f32 v[54:55], v[52:53], s[0:1], v[122:123] op_sel_hi:[1,0,0]
	v_exp_f32_e32 v57, v57
	v_pk_fma_f32 v[54:55], v[52:53], v[54:55], s[14:15] op_sel_hi:[1,1,0]
	v_and_b32_e32 v59, 0x7fffffff, v31
	v_pk_fma_f32 v[54:55], v[52:53], v[54:55], s[6:7] op_sel_hi:[1,1,0]
	v_and_b32_e32 v58, 0x7fffffff, v30
	v_pk_fma_f32 v[54:55], v[52:53], v[54:55], s[10:11] op_sel_hi:[1,1,0]
	v_pk_fma_f32 v[58:59], v[58:59], s[8:9], 1.0 op_sel_hi:[1,0,0]
	v_pk_mul_f32 v[52:53], v[52:53], v[54:55]
	v_rcp_f32_e32 v58, v58
	v_rcp_f32_e32 v59, v59
	v_pk_mul_f32 v[52:53], v[56:57], v[52:53]
	v_cmp_gt_f32_e32 vcc, 0, v28
	v_pk_mul_f32 v[56:57], v[28:29], v[52:53]
	v_pk_fma_f32 v[52:53], v[28:29], v[52:53], v[28:29] neg_lo:[1,0,0] neg_hi:[1,0,0]
	v_pk_mul_f32 v[54:55], v[30:31], v[30:31]
	v_cndmask_b32_e32 v56, v52, v56, vcc
	v_cmp_gt_f32_e32 vcc, 0, v29
	v_pk_fma_f32 v[28:29], v[58:59], s[0:1], v[122:123] op_sel_hi:[1,0,0]
	v_pk_fma_f32 v[24:25], v[40:41], v[62:63], v[24:25] op_sel_hi:[1,0,1] neg_lo:[1,0,0] neg_hi:[1,0,0]
	v_cndmask_b32_e32 v57, v53, v57, vcc
	v_pk_mul_f32 v[52:53], v[54:55], s[16:17] op_sel_hi:[1,0]
	v_pk_fma_f32 v[28:29], v[58:59], v[28:29], s[14:15] op_sel_hi:[1,1,0]
	v_exp_f32_e32 v52, v52
	v_exp_f32_e32 v53, v53
	v_pk_fma_f32 v[28:29], v[58:59], v[28:29], s[6:7] op_sel_hi:[1,1,0]
	v_cmp_gt_f32_e32 vcc, 0, v30
	v_pk_fma_f32 v[28:29], v[58:59], v[28:29], s[10:11] op_sel_hi:[1,1,0]
	v_pk_fma_f32 v[24:25], v[62:63], v[24:25], v[36:37] op_sel:[1,0,0]
	v_pk_mul_f32 v[28:29], v[58:59], v[28:29]
	v_pk_mul_f32 v[54:55], v[24:25], v[24:25]
	v_pk_mul_f32 v[28:29], v[52:53], v[28:29]
	v_pk_fma_f32 v[26:27], v[42:43], v[62:63], v[26:27] op_sel_hi:[1,0,1]
	v_pk_mul_f32 v[52:53], v[30:31], v[28:29]
	v_pk_fma_f32 v[28:29], v[30:31], v[28:29], v[30:31] neg_lo:[1,0,0] neg_hi:[1,0,0]
	v_and_b32_e32 v30, 0x7fffffff, v24
	v_cndmask_b32_e32 v52, v28, v52, vcc
	v_cmp_gt_f32_e32 vcc, 0, v31
	v_and_b32_e32 v31, 0x7fffffff, v25
	v_pk_fma_f32 v[30:31], v[30:31], s[8:9], 1.0 op_sel_hi:[1,0,0]
	v_cndmask_b32_e32 v29, v29, v53, vcc
	v_rcp_f32_e32 v30, v30
	v_rcp_f32_e32 v31, v31
	v_cvt_pk_f16_f32 v29, v52, v29
	v_pk_mul_f32 v[54:55], v[54:55], s[16:17] op_sel_hi:[1,0]
	v_pk_fma_f32 v[26:27], v[62:63], v[26:27], v[38:39] op_sel:[1,0,0]
	v_pk_fma_f32 v[52:53], v[30:31], s[0:1], v[122:123] op_sel_hi:[1,0,0]
	v_exp_f32_e32 v54, v54
	v_pk_fma_f32 v[52:53], v[30:31], v[52:53], s[14:15] op_sel_hi:[1,1,0]
	v_exp_f32_e32 v55, v55
	v_cvt_pk_f16_f32 v28, v56, v57
	v_pk_fma_f32 v[52:53], v[30:31], v[52:53], s[6:7] op_sel_hi:[1,1,0]
	v_and_b32_e32 v57, 0x7fffffff, v27
	v_and_b32_e32 v56, 0x7fffffff, v26
	v_pk_fma_f32 v[52:53], v[30:31], v[52:53], s[10:11] op_sel_hi:[1,1,0]
	v_pk_fma_f32 v[56:57], v[56:57], s[8:9], 1.0 op_sel_hi:[1,0,0]
	v_pk_mul_f32 v[30:31], v[30:31], v[52:53]
	v_rcp_f32_e32 v56, v56
	v_rcp_f32_e32 v57, v57
	v_pk_mul_f32 v[30:31], v[54:55], v[30:31]
	v_cmp_gt_f32_e32 vcc, 0, v24
	v_pk_mul_f32 v[54:55], v[24:25], v[30:31]
	v_pk_fma_f32 v[30:31], v[24:25], v[30:31], v[24:25] neg_lo:[1,0,0] neg_hi:[1,0,0]
	v_pk_mul_f32 v[52:53], v[26:27], v[26:27]
	v_cndmask_b32_e32 v54, v30, v54, vcc
	v_cmp_gt_f32_e32 vcc, 0, v25
	v_pk_fma_f32 v[24:25], v[56:57], s[0:1], v[122:123] op_sel_hi:[1,0,0]
	v_pk_fma_f32 v[20:21], v[40:41], v[44:45], v[20:21] op_sel_hi:[1,0,1] neg_lo:[1,0,0] neg_hi:[1,0,0]
	v_cndmask_b32_e32 v55, v31, v55, vcc
	v_pk_mul_f32 v[30:31], v[52:53], s[16:17] op_sel_hi:[1,0]
	v_pk_fma_f32 v[24:25], v[56:57], v[24:25], s[14:15] op_sel_hi:[1,1,0]
	v_exp_f32_e32 v30, v30
	v_exp_f32_e32 v31, v31
	v_pk_fma_f32 v[24:25], v[56:57], v[24:25], s[6:7] op_sel_hi:[1,1,0]
	v_cmp_gt_f32_e32 vcc, 0, v26
	v_pk_fma_f32 v[24:25], v[56:57], v[24:25], s[10:11] op_sel_hi:[1,1,0]
	v_pk_fma_f32 v[20:21], v[44:45], v[20:21], v[36:37] op_sel:[1,0,0]
	v_pk_mul_f32 v[24:25], v[56:57], v[24:25]
	v_pk_mul_f32 v[52:53], v[20:21], v[20:21]
	v_pk_mul_f32 v[24:25], v[30:31], v[24:25]
	v_pk_fma_f32 v[22:23], v[42:43], v[44:45], v[22:23] op_sel_hi:[1,0,1]
	v_pk_mul_f32 v[30:31], v[26:27], v[24:25]
	v_pk_fma_f32 v[24:25], v[26:27], v[24:25], v[26:27] neg_lo:[1,0,0] neg_hi:[1,0,0]
	v_and_b32_e32 v26, 0x7fffffff, v20
	v_cndmask_b32_e32 v30, v24, v30, vcc
	v_cmp_gt_f32_e32 vcc, 0, v27
	v_and_b32_e32 v27, 0x7fffffff, v21
	v_pk_fma_f32 v[26:27], v[26:27], s[8:9], 1.0 op_sel_hi:[1,0,0]
	v_cndmask_b32_e32 v25, v25, v31, vcc
	v_rcp_f32_e32 v26, v26
	v_rcp_f32_e32 v27, v27
	v_cvt_pk_f16_f32 v25, v30, v25
	v_pk_mul_f32 v[52:53], v[52:53], s[16:17] op_sel_hi:[1,0]
	v_pk_fma_f32 v[22:23], v[44:45], v[22:23], v[38:39] op_sel:[1,0,0]
	v_pk_fma_f32 v[30:31], v[26:27], s[0:1], v[122:123] op_sel_hi:[1,0,0]
	v_exp_f32_e32 v52, v52
	v_pk_fma_f32 v[30:31], v[26:27], v[30:31], s[14:15] op_sel_hi:[1,1,0]
	v_exp_f32_e32 v53, v53
	v_cvt_pk_f16_f32 v24, v54, v55
	v_pk_fma_f32 v[30:31], v[26:27], v[30:31], s[6:7] op_sel_hi:[1,1,0]
	v_and_b32_e32 v55, 0x7fffffff, v23
	v_and_b32_e32 v54, 0x7fffffff, v22
	v_pk_fma_f32 v[30:31], v[26:27], v[30:31], s[10:11] op_sel_hi:[1,1,0]
	v_pk_fma_f32 v[54:55], v[54:55], s[8:9], 1.0 op_sel_hi:[1,0,0]
	v_pk_mul_f32 v[26:27], v[26:27], v[30:31]
	v_rcp_f32_e32 v54, v54
	v_rcp_f32_e32 v55, v55
	v_pk_mul_f32 v[26:27], v[52:53], v[26:27]
	v_cmp_gt_f32_e32 vcc, 0, v20
	v_pk_mul_f32 v[52:53], v[20:21], v[26:27]
	v_pk_fma_f32 v[26:27], v[20:21], v[26:27], v[20:21] neg_lo:[1,0,0] neg_hi:[1,0,0]
	v_pk_mul_f32 v[30:31], v[22:23], v[22:23]
	v_cndmask_b32_e32 v52, v26, v52, vcc
	v_cmp_gt_f32_e32 vcc, 0, v21
	v_pk_fma_f32 v[20:21], v[54:55], s[0:1], v[122:123] op_sel_hi:[1,0,0]
	v_pk_fma_f32 v[16:17], v[40:41], v[46:47], v[16:17] op_sel_hi:[1,0,1] neg_lo:[1,0,0] neg_hi:[1,0,0]
	v_cndmask_b32_e32 v53, v27, v53, vcc
	v_pk_mul_f32 v[26:27], v[30:31], s[16:17] op_sel_hi:[1,0]
	v_pk_fma_f32 v[20:21], v[54:55], v[20:21], s[14:15] op_sel_hi:[1,1,0]
	v_exp_f32_e32 v26, v26
	v_exp_f32_e32 v27, v27
	v_pk_fma_f32 v[20:21], v[54:55], v[20:21], s[6:7] op_sel_hi:[1,1,0]
	v_cmp_gt_f32_e32 vcc, 0, v22
	v_pk_fma_f32 v[20:21], v[54:55], v[20:21], s[10:11] op_sel_hi:[1,1,0]
	v_pk_fma_f32 v[16:17], v[46:47], v[16:17], v[36:37] op_sel:[1,0,0]
	v_pk_mul_f32 v[20:21], v[54:55], v[20:21]
	v_pk_mul_f32 v[30:31], v[16:17], v[16:17]
	v_pk_mul_f32 v[20:21], v[26:27], v[20:21]
	v_pk_fma_f32 v[18:19], v[42:43], v[46:47], v[18:19] op_sel_hi:[1,0,1]
	v_pk_mul_f32 v[26:27], v[22:23], v[20:21]
	v_pk_fma_f32 v[20:21], v[22:23], v[20:21], v[22:23] neg_lo:[1,0,0] neg_hi:[1,0,0]
	v_and_b32_e32 v22, 0x7fffffff, v16
	v_cndmask_b32_e32 v26, v20, v26, vcc
	v_cmp_gt_f32_e32 vcc, 0, v23
	v_and_b32_e32 v23, 0x7fffffff, v17
	v_pk_fma_f32 v[22:23], v[22:23], s[8:9], 1.0 op_sel_hi:[1,0,0]
	v_cndmask_b32_e32 v21, v21, v27, vcc
	v_rcp_f32_e32 v22, v22
	v_rcp_f32_e32 v23, v23
	v_cvt_pk_f16_f32 v21, v26, v21
	v_pk_mul_f32 v[30:31], v[30:31], s[16:17] op_sel_hi:[1,0]
	v_pk_fma_f32 v[18:19], v[46:47], v[18:19], v[38:39] op_sel:[1,0,0]
	v_pk_fma_f32 v[26:27], v[22:23], s[0:1], v[122:123] op_sel_hi:[1,0,0]
	v_exp_f32_e32 v30, v30
	v_pk_fma_f32 v[26:27], v[22:23], v[26:27], s[14:15] op_sel_hi:[1,1,0]
	v_exp_f32_e32 v31, v31
	v_pk_fma_f32 v[26:27], v[22:23], v[26:27], s[6:7] op_sel_hi:[1,1,0]
	v_and_b32_e32 v37, 0x7fffffff, v19
	v_and_b32_e32 v36, 0x7fffffff, v18
	v_pk_fma_f32 v[26:27], v[22:23], v[26:27], s[10:11] op_sel_hi:[1,1,0]
	v_pk_fma_f32 v[36:37], v[36:37], s[8:9], 1.0 op_sel_hi:[1,0,0]
	v_pk_mul_f32 v[22:23], v[22:23], v[26:27]
	v_rcp_f32_e32 v36, v36
	v_rcp_f32_e32 v37, v37
	v_pk_mul_f32 v[22:23], v[30:31], v[22:23]
	v_cmp_gt_f32_e32 vcc, 0, v16
	v_pk_mul_f32 v[30:31], v[16:17], v[22:23]
	v_pk_fma_f32 v[22:23], v[16:17], v[22:23], v[16:17] neg_lo:[1,0,0] neg_hi:[1,0,0]
	v_pk_mul_f32 v[26:27], v[18:19], v[18:19]
	v_cndmask_b32_e32 v30, v22, v30, vcc
	v_cmp_gt_f32_e32 vcc, 0, v17
	v_pk_fma_f32 v[16:17], v[36:37], s[0:1], v[122:123] op_sel_hi:[1,0,0]
	s_waitcnt vmcnt(1)
	v_pk_fma_f32 v[8:9], v[48:49], v[62:63], v[8:9] op_sel_hi:[1,0,1] neg_lo:[1,0,0] neg_hi:[1,0,0]
	v_cndmask_b32_e32 v31, v23, v31, vcc
	v_pk_mul_f32 v[22:23], v[26:27], s[16:17] op_sel_hi:[1,0]
	v_pk_fma_f32 v[16:17], v[36:37], v[16:17], s[14:15] op_sel_hi:[1,1,0]
	v_exp_f32_e32 v22, v22
	v_exp_f32_e32 v23, v23
	v_pk_fma_f32 v[16:17], v[36:37], v[16:17], s[6:7] op_sel_hi:[1,1,0]
	v_cmp_gt_f32_e32 vcc, 0, v18
	v_pk_fma_f32 v[16:17], v[36:37], v[16:17], s[10:11] op_sel_hi:[1,1,0]
	s_waitcnt vmcnt(0)
	v_pk_fma_f32 v[8:9], v[62:63], v[8:9], v[32:33] op_sel:[1,0,0]
	v_pk_mul_f32 v[16:17], v[36:37], v[16:17]
	v_pk_fma_f32 v[4:5], v[48:49], v[44:45], v[4:5] op_sel_hi:[1,0,1] neg_lo:[1,0,0] neg_hi:[1,0,0]
	v_pk_mul_f32 v[16:17], v[22:23], v[16:17]
	v_pk_fma_f32 v[4:5], v[44:45], v[4:5], v[32:33] op_sel:[1,0,0]
	v_pk_mul_f32 v[22:23], v[18:19], v[16:17]
	v_pk_fma_f32 v[16:17], v[18:19], v[16:17], v[18:19] neg_lo:[1,0,0] neg_hi:[1,0,0]
	v_pk_fma_f32 v[0:1], v[48:49], v[46:47], v[0:1] op_sel_hi:[1,0,1] neg_lo:[1,0,0] neg_hi:[1,0,0]
	v_cndmask_b32_e32 v18, v16, v22, vcc
	v_cmp_gt_f32_e32 vcc, 0, v19
	v_cvt_pk_f16_f32 v16, v30, v31
	v_pk_fma_f32 v[0:1], v[46:47], v[0:1], v[32:33] op_sel:[1,0,0]
	v_cndmask_b32_e32 v17, v17, v23, vcc
	v_cvt_pk_f16_f32 v17, v18, v17
	v_pk_fma_f32 v[18:19], v[48:49], v[60:61], v[12:13] op_sel_hi:[1,0,1] neg_lo:[1,0,0] neg_hi:[1,0,0]
	v_xor_b32_e32 v13, 0x80000000, v51
	v_pk_fma_f32 v[18:19], v[60:61], v[18:19], v[32:33] op_sel:[1,0,0]
	v_xor_b32_e32 v12, 0x80000000, v50
	v_and_b32_e32 v23, 0x7fffffff, v19
	v_and_b32_e32 v22, 0x7fffffff, v18
	v_pk_fma_f32 v[22:23], v[22:23], s[8:9], 1.0 op_sel_hi:[1,0,0]
	v_pk_mul_f32 v[30:31], v[18:19], v[18:19]
	v_rcp_f32_e32 v22, v22
	v_rcp_f32_e32 v23, v23
	v_pk_fma_f32 v[14:15], v[12:13], v[60:61], v[14:15] op_sel_hi:[1,0,1]
	v_pk_mul_f32 v[30:31], v[30:31], s[16:17] op_sel_hi:[1,0]
	v_pk_fma_f32 v[14:15], v[60:61], v[14:15], v[34:35] op_sel:[1,0,0]
	v_pk_fma_f32 v[26:27], v[22:23], s[0:1], v[122:123] op_sel_hi:[1,0,0]
	v_exp_f32_e32 v30, v30
	v_pk_fma_f32 v[26:27], v[22:23], v[26:27], s[14:15] op_sel_hi:[1,1,0]
	v_exp_f32_e32 v31, v31
	v_pk_fma_f32 v[26:27], v[22:23], v[26:27], s[6:7] op_sel_hi:[1,1,0]
	v_and_b32_e32 v37, 0x7fffffff, v15
	v_and_b32_e32 v36, 0x7fffffff, v14
	v_pk_fma_f32 v[26:27], v[22:23], v[26:27], s[10:11] op_sel_hi:[1,1,0]
	v_pk_fma_f32 v[36:37], v[36:37], s[8:9], 1.0 op_sel_hi:[1,0,0]
	v_pk_mul_f32 v[22:23], v[22:23], v[26:27]
	v_rcp_f32_e32 v36, v36
	v_rcp_f32_e32 v37, v37
	v_pk_mul_f32 v[22:23], v[30:31], v[22:23]
	v_cmp_gt_f32_e32 vcc, 0, v18
	v_pk_mul_f32 v[30:31], v[18:19], v[22:23]
	v_pk_fma_f32 v[22:23], v[18:19], v[22:23], v[18:19] neg_lo:[1,0,0] neg_hi:[1,0,0]
	v_pk_mul_f32 v[26:27], v[14:15], v[14:15]
	v_cndmask_b32_e32 v30, v22, v30, vcc
	v_cmp_gt_f32_e32 vcc, 0, v19
	v_pk_fma_f32 v[18:19], v[36:37], s[0:1], v[122:123] op_sel_hi:[1,0,0]
	v_pk_fma_f32 v[10:11], v[12:13], v[62:63], v[10:11] op_sel_hi:[1,0,1]
	v_cndmask_b32_e32 v31, v23, v31, vcc
	v_pk_mul_f32 v[22:23], v[26:27], s[16:17] op_sel_hi:[1,0]
	v_pk_fma_f32 v[18:19], v[36:37], v[18:19], s[14:15] op_sel_hi:[1,1,0]
	v_exp_f32_e32 v22, v22
	v_exp_f32_e32 v23, v23
	v_pk_fma_f32 v[18:19], v[36:37], v[18:19], s[6:7] op_sel_hi:[1,1,0]
	v_cmp_gt_f32_e32 vcc, 0, v14
	v_pk_fma_f32 v[18:19], v[36:37], v[18:19], s[10:11] op_sel_hi:[1,1,0]
	v_pk_fma_f32 v[10:11], v[62:63], v[10:11], v[34:35] op_sel:[1,0,0]
	v_pk_mul_f32 v[18:19], v[36:37], v[18:19]
	v_and_b32_e32 v27, 0x7fffffff, v11
	v_pk_mul_f32 v[18:19], v[22:23], v[18:19]
	v_and_b32_e32 v26, 0x7fffffff, v10
	v_pk_mul_f32 v[22:23], v[14:15], v[18:19]
	v_pk_fma_f32 v[18:19], v[14:15], v[18:19], v[14:15] neg_lo:[1,0,0] neg_hi:[1,0,0]
	v_cvt_pk_f16_f32 v14, v30, v31
	v_cndmask_b32_e32 v18, v18, v22, vcc
	v_cmp_gt_f32_e32 vcc, 0, v15
	v_pk_fma_f32 v[26:27], v[26:27], s[8:9], 1.0 op_sel_hi:[1,0,0]
	v_pk_fma_f32 v[6:7], v[12:13], v[44:45], v[6:7] op_sel_hi:[1,0,1]
	v_cndmask_b32_e32 v15, v19, v23, vcc
	v_cvt_pk_f16_f32 v15, v18, v15
	v_and_b32_e32 v19, 0x7fffffff, v9
	v_and_b32_e32 v18, 0x7fffffff, v8
	v_pk_fma_f32 v[18:19], v[18:19], s[8:9], 1.0 op_sel_hi:[1,0,0]
	v_pk_mul_f32 v[22:23], v[8:9], v[8:9]
	v_rcp_f32_e32 v18, v18
	v_rcp_f32_e32 v19, v19
	ds_write2_b64 v121, v[28:29], v[14:15] offset0:16 offset1:20
	v_pk_mul_f32 v[22:23], v[22:23], s[16:17] op_sel_hi:[1,0]
	v_rcp_f32_e32 v26, v26
	v_pk_fma_f32 v[14:15], v[18:19], s[0:1], v[122:123] op_sel_hi:[1,0,0]
	v_exp_f32_e32 v22, v22
	v_pk_fma_f32 v[14:15], v[18:19], v[14:15], s[14:15] op_sel_hi:[1,1,0]
	v_exp_f32_e32 v23, v23
	v_pk_fma_f32 v[14:15], v[18:19], v[14:15], s[6:7] op_sel_hi:[1,1,0]
	v_rcp_f32_e32 v27, v27
	v_pk_fma_f32 v[14:15], v[18:19], v[14:15], s[10:11] op_sel_hi:[1,1,0]
	v_cmp_gt_f32_e32 vcc, 0, v8
	v_pk_mul_f32 v[14:15], v[18:19], v[14:15]
	v_pk_mul_f32 v[18:19], v[10:11], v[10:11]
	v_pk_mul_f32 v[14:15], v[22:23], v[14:15]
	v_pk_fma_f32 v[6:7], v[44:45], v[6:7], v[34:35] op_sel:[1,0,0]
	v_pk_mul_f32 v[22:23], v[8:9], v[14:15]
	v_pk_fma_f32 v[14:15], v[8:9], v[14:15], v[8:9] neg_lo:[1,0,0] neg_hi:[1,0,0]
	v_cvt_pk_f16_f32 v20, v52, v53
	v_cndmask_b32_e32 v22, v14, v22, vcc
	v_cmp_gt_f32_e32 vcc, 0, v9
	v_pk_fma_f32 v[8:9], v[26:27], s[0:1], v[122:123] op_sel_hi:[1,0,0]
	v_pk_fma_f32 v[2:3], v[12:13], v[46:47], v[2:3] op_sel_hi:[1,0,1]
	v_cndmask_b32_e32 v23, v15, v23, vcc
	v_pk_mul_f32 v[14:15], v[18:19], s[16:17] op_sel_hi:[1,0]
	v_pk_fma_f32 v[8:9], v[26:27], v[8:9], s[14:15] op_sel_hi:[1,1,0]
	v_exp_f32_e32 v14, v14
	v_exp_f32_e32 v15, v15
	v_pk_fma_f32 v[8:9], v[26:27], v[8:9], s[6:7] op_sel_hi:[1,1,0]
	v_cmp_gt_f32_e32 vcc, 0, v10
	v_pk_fma_f32 v[8:9], v[26:27], v[8:9], s[10:11] op_sel_hi:[1,1,0]
	v_and_b32_e32 v19, 0x7fffffff, v7
	v_pk_mul_f32 v[8:9], v[26:27], v[8:9]
	v_and_b32_e32 v18, 0x7fffffff, v6
	v_pk_mul_f32 v[8:9], v[14:15], v[8:9]
	v_pk_fma_f32 v[18:19], v[18:19], s[8:9], 1.0 op_sel_hi:[1,0,0]
	v_pk_mul_f32 v[14:15], v[10:11], v[8:9]
	v_pk_fma_f32 v[8:9], v[10:11], v[8:9], v[10:11] neg_lo:[1,0,0] neg_hi:[1,0,0]
	v_rcp_f32_e32 v18, v18
	v_cndmask_b32_e32 v10, v8, v14, vcc
	v_cmp_gt_f32_e32 vcc, 0, v11
	v_and_b32_e32 v11, 0x7fffffff, v5
	v_cvt_pk_f16_f32 v8, v22, v23
	v_cndmask_b32_e32 v9, v9, v15, vcc
	v_cvt_pk_f16_f32 v9, v10, v9
	v_and_b32_e32 v10, 0x7fffffff, v4
	v_pk_fma_f32 v[10:11], v[10:11], s[8:9], 1.0 op_sel_hi:[1,0,0]
	v_pk_mul_f32 v[14:15], v[4:5], v[4:5]
	v_rcp_f32_e32 v10, v10
	v_rcp_f32_e32 v11, v11
	ds_write2_b64 v94, v[24:25], v[8:9] offset0:48 offset1:52
	v_pk_mul_f32 v[14:15], v[14:15], s[16:17] op_sel_hi:[1,0]
	v_rcp_f32_e32 v19, v19
	v_pk_fma_f32 v[8:9], v[10:11], s[0:1], v[122:123] op_sel_hi:[1,0,0]
	v_exp_f32_e32 v14, v14
	v_pk_fma_f32 v[8:9], v[10:11], v[8:9], s[14:15] op_sel_hi:[1,1,0]
	v_exp_f32_e32 v15, v15
	v_pk_fma_f32 v[8:9], v[10:11], v[8:9], s[6:7] op_sel_hi:[1,1,0]
	v_cmp_gt_f32_e32 vcc, 0, v4
	v_pk_fma_f32 v[8:9], v[10:11], v[8:9], s[10:11] op_sel_hi:[1,1,0]
	v_pk_fma_f32 v[2:3], v[46:47], v[2:3], v[34:35] op_sel:[1,0,0]
	v_pk_mul_f32 v[8:9], v[10:11], v[8:9]
	v_pk_mul_f32 v[10:11], v[6:7], v[6:7]
	v_pk_mul_f32 v[8:9], v[14:15], v[8:9]
	s_nop 0
	v_pk_mul_f32 v[14:15], v[4:5], v[8:9]
	v_pk_fma_f32 v[8:9], v[4:5], v[8:9], v[4:5] neg_lo:[1,0,0] neg_hi:[1,0,0]
	s_nop 0
	v_cndmask_b32_e32 v14, v8, v14, vcc
	v_cmp_gt_f32_e32 vcc, 0, v5
	v_pk_fma_f32 v[4:5], v[18:19], s[0:1], v[122:123] op_sel_hi:[1,0,0]
	s_nop 0
	v_cndmask_b32_e32 v15, v9, v15, vcc
	v_pk_mul_f32 v[8:9], v[10:11], s[16:17] op_sel_hi:[1,0]
	v_pk_fma_f32 v[4:5], v[18:19], v[4:5], s[14:15] op_sel_hi:[1,1,0]
	v_exp_f32_e32 v8, v8
	v_exp_f32_e32 v9, v9
	v_pk_fma_f32 v[4:5], v[18:19], v[4:5], s[6:7] op_sel_hi:[1,1,0]
	v_cmp_gt_f32_e32 vcc, 0, v6
	v_pk_fma_f32 v[4:5], v[18:19], v[4:5], s[10:11] op_sel_hi:[1,1,0]
	v_and_b32_e32 v11, 0x7fffffff, v3
	v_pk_mul_f32 v[4:5], v[18:19], v[4:5]
	v_and_b32_e32 v10, 0x7fffffff, v2
	v_pk_mul_f32 v[4:5], v[8:9], v[4:5]
	v_pk_fma_f32 v[10:11], v[10:11], s[8:9], 1.0 op_sel_hi:[1,0,0]
	v_pk_mul_f32 v[8:9], v[6:7], v[4:5]
	v_pk_fma_f32 v[4:5], v[6:7], v[4:5], v[6:7] neg_lo:[1,0,0] neg_hi:[1,0,0]
	v_rcp_f32_e32 v10, v10
	v_cndmask_b32_e32 v6, v4, v8, vcc
	v_cmp_gt_f32_e32 vcc, 0, v7
	v_and_b32_e32 v7, 0x7fffffff, v1
	v_cvt_pk_f16_f32 v4, v14, v15
	v_cndmask_b32_e32 v5, v5, v9, vcc
	v_cvt_pk_f16_f32 v5, v6, v5
	v_and_b32_e32 v6, 0x7fffffff, v0
	v_pk_fma_f32 v[6:7], v[6:7], s[8:9], 1.0 op_sel_hi:[1,0,0]
	v_pk_mul_f32 v[8:9], v[0:1], v[0:1]
	v_rcp_f32_e32 v6, v6
	v_rcp_f32_e32 v7, v7
	ds_write2_b64 v95, v[20:21], v[4:5] offset0:80 offset1:84
	v_pk_mul_f32 v[8:9], v[8:9], s[16:17] op_sel_hi:[1,0]
	v_rcp_f32_e32 v11, v11
	v_pk_fma_f32 v[4:5], v[6:7], s[0:1], v[122:123] op_sel_hi:[1,0,0]
	v_exp_f32_e32 v8, v8
	v_pk_fma_f32 v[4:5], v[6:7], v[4:5], s[14:15] op_sel_hi:[1,1,0]
	v_exp_f32_e32 v9, v9
	v_pk_fma_f32 v[4:5], v[6:7], v[4:5], s[6:7] op_sel_hi:[1,1,0]
	v_cmp_gt_f32_e32 vcc, 0, v0
	v_pk_fma_f32 v[4:5], v[6:7], v[4:5], s[10:11] op_sel_hi:[1,1,0]
	s_nop 0
	v_pk_mul_f32 v[4:5], v[6:7], v[4:5]
	v_pk_mul_f32 v[6:7], v[2:3], v[2:3]
	v_pk_mul_f32 v[4:5], v[8:9], v[4:5]
	s_nop 0
	v_pk_mul_f32 v[8:9], v[0:1], v[4:5]
	v_pk_fma_f32 v[4:5], v[0:1], v[4:5], v[0:1] neg_lo:[1,0,0] neg_hi:[1,0,0]
	s_nop 0
	v_cndmask_b32_e32 v8, v4, v8, vcc
	v_cmp_gt_f32_e32 vcc, 0, v1
	v_pk_fma_f32 v[0:1], v[10:11], s[0:1], v[122:123] op_sel_hi:[1,0,0]
	s_lshl_b64 s[0:1], s[2:3], 1
	v_cndmask_b32_e32 v9, v5, v9, vcc
	v_pk_mul_f32 v[4:5], v[6:7], s[16:17] op_sel_hi:[1,0]
	v_pk_fma_f32 v[0:1], v[10:11], v[0:1], s[14:15] op_sel_hi:[1,1,0]
	v_exp_f32_e32 v4, v4
	v_exp_f32_e32 v5, v5
	v_pk_fma_f32 v[0:1], v[10:11], v[0:1], s[6:7] op_sel_hi:[1,1,0]
	v_cmp_gt_f32_e32 vcc, 0, v2
	v_pk_fma_f32 v[0:1], v[10:11], v[0:1], s[10:11] op_sel_hi:[1,1,0]
	s_mov_b32 s2, 0x2aaaaaab
	v_pk_mul_f32 v[0:1], v[10:11], v[0:1]
	s_add_u32 s0, s4, s0
	v_pk_mul_f32 v[0:1], v[4:5], v[0:1]
	s_movk_i32 s3, 0xffe8
	v_pk_mul_f32 v[4:5], v[2:3], v[0:1]
	v_pk_fma_f32 v[0:1], v[2:3], v[0:1], v[2:3] neg_lo:[1,0,0] neg_hi:[1,0,0]
	s_addc_u32 s1, s5, s1
	v_cndmask_b32_e32 v2, v0, v4, vcc
	v_cmp_gt_f32_e32 vcc, 0, v3
	v_cvt_pk_f16_f32 v0, v8, v9
	s_nop 0
	v_cndmask_b32_e32 v1, v1, v5, vcc
	v_cvt_pk_f16_f32 v1, v2, v1
	ds_write2_b64 v90, v[16:17], v[0:1] offset0:112 offset1:116
	v_mul_hi_i32 v0, v120, s2
	v_lshrrev_b32_e32 v1, 31, v0
	v_ashrrev_i32_e32 v0, 2, v0
	v_add_u32_e32 v6, v0, v1
	v_mad_u64_u32 v[4:5], s[4:5], v6, s3, v[120:121]
	v_add_u32_e32 v5, s17, v6
	v_mul_lo_u32 v0, v6, s7
	v_lshlrev_b32_e32 v1, 4, v4
	v_mad_i64_i32 v[6:7], s[4:5], v5, s12, 0
	v_lshlrev_b32_e32 v4, 3, v4
	v_lshl_add_u64 v[6:7], v[6:7], 1, s[0:1]
	v_ashrrev_i32_e32 v5, 31, v4
	v_lshl_add_u64 v[8:9], v[4:5], 1, v[6:7]
	v_add_u32_e32 v4, 0x100, v120
	v_mul_hi_i32 v5, v4, s2
	s_waitcnt lgkmcnt(0)
	s_barrier
	v_add3_u32 v0, 0, v0, v1
	v_lshrrev_b32_e32 v6, 31, v5
	v_ashrrev_i32_e32 v5, 2, v5
	ds_read_b128 v[0:3], v0
	v_add_u32_e32 v12, v5, v6
	v_mad_u64_u32 v[10:11], s[4:5], v12, s3, v[4:5]
	v_mul_lo_u32 v4, v12, s7
	v_lshlrev_b32_e32 v5, 4, v10
	v_add3_u32 v4, 0, v4, v5
	ds_read_b128 v[4:7], v4
	s_waitcnt lgkmcnt(1)
	global_store_dwordx4 v[8:9], v[0:3], off sc0 sc1
	s_nop 1
	v_add_u32_e32 v0, s17, v12
	v_mad_i64_i32 v[0:1], s[4:5], v0, s12, 0
	v_lshlrev_b32_e32 v2, 3, v10
	v_lshl_add_u64 v[0:1], v[0:1], 1, s[0:1]
	v_ashrrev_i32_e32 v3, 31, v2
	v_lshl_add_u64 v[0:1], v[2:3], 1, v[0:1]
	s_waitcnt lgkmcnt(0)
	global_store_dwordx4 v[0:1], v[4:7], off sc0 sc1
	v_add_u32_e32 v0, 0x200, v120
	v_mul_hi_i32 v1, v0, s2
	v_lshrrev_b32_e32 v2, 31, v1
	v_ashrrev_i32_e32 v1, 2, v1
	v_add_u32_e32 v6, v1, v2
	v_mad_u64_u32 v[4:5], s[4:5], v6, s3, v[0:1]
	v_add_u32_e32 v5, s17, v6
	v_mul_lo_u32 v0, v6, s7
	v_lshlrev_b32_e32 v1, 4, v4
	v_mad_i64_i32 v[6:7], s[4:5], v5, s12, 0
	v_lshlrev_b32_e32 v4, 3, v4
	v_lshl_add_u64 v[6:7], v[6:7], 1, s[0:1]
	v_ashrrev_i32_e32 v5, 31, v4
	v_lshl_add_u64 v[8:9], v[4:5], 1, v[6:7]
	v_add_u32_e32 v4, 0x300, v120
	v_mul_hi_i32 v5, v4, s2
	v_add3_u32 v0, 0, v0, v1
	v_lshrrev_b32_e32 v6, 31, v5
	v_ashrrev_i32_e32 v5, 2, v5
	ds_read_b128 v[0:3], v0
	v_add_u32_e32 v12, v5, v6
	v_mad_u64_u32 v[10:11], s[4:5], v12, s3, v[4:5]
	v_mul_lo_u32 v4, v12, s7
	v_lshlrev_b32_e32 v5, 4, v10
	v_add3_u32 v4, 0, v4, v5
	ds_read_b128 v[4:7], v4
	s_waitcnt lgkmcnt(1)
	global_store_dwordx4 v[8:9], v[0:3], off sc0 sc1
	s_nop 1
	v_add_u32_e32 v0, s17, v12
	v_mad_i64_i32 v[0:1], s[4:5], v0, s12, 0
	v_lshlrev_b32_e32 v2, 3, v10
	v_lshl_add_u64 v[0:1], v[0:1], 1, s[0:1]
	v_ashrrev_i32_e32 v3, 31, v2
	v_lshl_add_u64 v[0:1], v[2:3], 1, v[0:1]
	s_waitcnt lgkmcnt(0)
	global_store_dwordx4 v[0:1], v[4:7], off sc0 sc1
	v_add_u32_e32 v0, 0x400, v120
	v_mul_hi_i32 v1, v0, s2
	v_lshrrev_b32_e32 v2, 31, v1
	v_ashrrev_i32_e32 v1, 2, v1
	v_add_u32_e32 v6, v1, v2
	v_mad_u64_u32 v[4:5], s[4:5], v6, s3, v[0:1]
	v_add_u32_e32 v5, s17, v6
	v_mul_lo_u32 v0, v6, s7
	v_lshlrev_b32_e32 v1, 4, v4
	v_mad_i64_i32 v[6:7], s[4:5], v5, s12, 0
	v_lshlrev_b32_e32 v4, 3, v4
	v_lshl_add_u64 v[6:7], v[6:7], 1, s[0:1]
	v_ashrrev_i32_e32 v5, 31, v4
	v_lshl_add_u64 v[8:9], v[4:5], 1, v[6:7]
	v_add_u32_e32 v4, 0x500, v120
	v_mul_hi_i32 v5, v4, s2
	v_add3_u32 v0, 0, v0, v1
	v_lshrrev_b32_e32 v6, 31, v5
	v_ashrrev_i32_e32 v5, 2, v5
	ds_read_b128 v[0:3], v0
	v_add_u32_e32 v12, v5, v6
	v_mad_u64_u32 v[10:11], s[4:5], v12, s3, v[4:5]
	v_mul_lo_u32 v4, v12, s7
	v_lshlrev_b32_e32 v5, 4, v10
	v_add3_u32 v4, 0, v4, v5
	ds_read_b128 v[4:7], v4
	s_waitcnt lgkmcnt(1)
	global_store_dwordx4 v[8:9], v[0:3], off sc0 sc1
	s_nop 1
	v_add_u32_e32 v0, s17, v12
	v_mad_i64_i32 v[0:1], s[4:5], v0, s12, 0
	v_lshlrev_b32_e32 v2, 3, v10
	v_lshl_add_u64 v[0:1], v[0:1], 1, s[0:1]
	v_ashrrev_i32_e32 v3, 31, v2
	v_lshl_add_u64 v[0:1], v[2:3], 1, v[0:1]
	s_waitcnt lgkmcnt(0)
	global_store_dwordx4 v[0:1], v[4:7], off sc0 sc1
	v_add_u32_e32 v0, 0x600, v120
	v_mul_hi_i32 v1, v0, s2
	v_lshrrev_b32_e32 v2, 31, v1
	v_ashrrev_i32_e32 v1, 2, v1
	v_add_u32_e32 v6, v1, v2
	v_mad_u64_u32 v[4:5], s[4:5], v6, s3, v[0:1]
	v_add_u32_e32 v5, s17, v6
	v_mul_lo_u32 v0, v6, s7
	v_lshlrev_b32_e32 v1, 4, v4
	v_mad_i64_i32 v[6:7], s[4:5], v5, s12, 0
	v_lshlrev_b32_e32 v4, 3, v4
	v_lshl_add_u64 v[6:7], v[6:7], 1, s[0:1]
	v_ashrrev_i32_e32 v5, 31, v4
	v_lshl_add_u64 v[8:9], v[4:5], 1, v[6:7]
	v_add_u32_e32 v4, 0x700, v120
	v_mul_hi_i32 v5, v4, s2
	v_add3_u32 v0, 0, v0, v1
	v_lshrrev_b32_e32 v6, 31, v5
	v_ashrrev_i32_e32 v5, 2, v5
	ds_read_b128 v[0:3], v0
	v_add_u32_e32 v12, v5, v6
	v_mad_u64_u32 v[10:11], s[4:5], v12, s3, v[4:5]
	v_mul_lo_u32 v4, v12, s7
	v_lshlrev_b32_e32 v5, 4, v10
	v_add3_u32 v4, 0, v4, v5
	ds_read_b128 v[4:7], v4
	s_waitcnt lgkmcnt(1)
	global_store_dwordx4 v[8:9], v[0:3], off sc0 sc1
	s_nop 1
	v_add_u32_e32 v0, s17, v12
	v_mad_i64_i32 v[0:1], s[4:5], v0, s12, 0
	v_lshlrev_b32_e32 v2, 3, v10
	v_lshl_add_u64 v[0:1], v[0:1], 1, s[0:1]
	v_ashrrev_i32_e32 v3, 31, v2
	v_lshl_add_u64 v[0:1], v[2:3], 1, v[0:1]
	s_waitcnt lgkmcnt(0)
	global_store_dwordx4 v[0:1], v[4:7], off sc0 sc1
	v_add_u32_e32 v0, 0x800, v120
	v_mul_hi_i32 v1, v0, s2
	v_lshrrev_b32_e32 v2, 31, v1
	v_ashrrev_i32_e32 v1, 2, v1
	v_add_u32_e32 v6, v1, v2
	v_mad_u64_u32 v[4:5], s[4:5], v6, s3, v[0:1]
	v_add_u32_e32 v5, s17, v6
	v_mul_lo_u32 v0, v6, s7
	v_lshlrev_b32_e32 v1, 4, v4
	v_mad_i64_i32 v[6:7], s[4:5], v5, s12, 0
	v_lshlrev_b32_e32 v4, 3, v4
	v_lshl_add_u64 v[6:7], v[6:7], 1, s[0:1]
	v_ashrrev_i32_e32 v5, 31, v4
	v_lshl_add_u64 v[8:9], v[4:5], 1, v[6:7]
	v_add_u32_e32 v4, 0x900, v120
	v_mul_hi_i32 v5, v4, s2
	v_add3_u32 v0, 0, v0, v1
	v_lshrrev_b32_e32 v6, 31, v5
	v_ashrrev_i32_e32 v5, 2, v5
	ds_read_b128 v[0:3], v0
	v_add_u32_e32 v12, v5, v6
	v_mad_u64_u32 v[10:11], s[4:5], v12, s3, v[4:5]
	v_mul_lo_u32 v4, v12, s7
	v_lshlrev_b32_e32 v5, 4, v10
	v_add3_u32 v4, 0, v4, v5
	ds_read_b128 v[4:7], v4
	s_waitcnt lgkmcnt(1)
	global_store_dwordx4 v[8:9], v[0:3], off sc0 sc1
	s_nop 1
	v_add_u32_e32 v0, s17, v12
	v_mad_i64_i32 v[0:1], s[4:5], v0, s12, 0
	v_lshlrev_b32_e32 v2, 3, v10
	v_lshl_add_u64 v[0:1], v[0:1], 1, s[0:1]
	v_ashrrev_i32_e32 v3, 31, v2
	v_lshl_add_u64 v[0:1], v[2:3], 1, v[0:1]
	s_waitcnt lgkmcnt(0)
	global_store_dwordx4 v[0:1], v[4:7], off sc0 sc1
	v_add_u32_e32 v0, 0xa00, v120
	v_mul_hi_i32 v1, v0, s2
	v_lshrrev_b32_e32 v2, 31, v1
	v_ashrrev_i32_e32 v1, 2, v1
	v_add_u32_e32 v6, v1, v2
	v_mad_u64_u32 v[4:5], s[4:5], v6, s3, v[0:1]
	v_add_u32_e32 v5, s17, v6
	v_mul_lo_u32 v0, v6, s7
	v_lshlrev_b32_e32 v1, 4, v4
	v_mad_i64_i32 v[6:7], s[4:5], v5, s12, 0
	v_lshlrev_b32_e32 v4, 3, v4
	v_lshl_add_u64 v[6:7], v[6:7], 1, s[0:1]
	v_ashrrev_i32_e32 v5, 31, v4
	v_lshl_add_u64 v[8:9], v[4:5], 1, v[6:7]
	v_add_u32_e32 v4, 0xb00, v120
	v_mul_hi_i32 v5, v4, s2
	v_add3_u32 v0, 0, v0, v1
	v_lshrrev_b32_e32 v6, 31, v5
	v_ashrrev_i32_e32 v5, 2, v5
	ds_read_b128 v[0:3], v0
	v_add_u32_e32 v12, v5, v6
	v_mad_u64_u32 v[10:11], s[2:3], v12, s3, v[4:5]
	v_mul_lo_u32 v4, v12, s7
	v_lshlrev_b32_e32 v5, 4, v10
	v_add3_u32 v4, 0, v4, v5
	ds_read_b128 v[4:7], v4
	s_waitcnt lgkmcnt(1)
	global_store_dwordx4 v[8:9], v[0:3], off sc0 sc1
	s_nop 1
	v_add_u32_e32 v0, s17, v12
	v_mad_i64_i32 v[0:1], s[2:3], v0, s12, 0
	v_lshlrev_b32_e32 v2, 3, v10
	v_lshl_add_u64 v[0:1], v[0:1], 1, s[0:1]
	v_ashrrev_i32_e32 v3, 31, v2
	v_lshl_add_u64 v[0:1], v[2:3], 1, v[0:1]
	s_waitcnt lgkmcnt(0)
	global_store_dwordx4 v[0:1], v[4:7], off sc0 sc1
	s_endpgm
	.p2align	8
